# phase-B loop edge: next delta fragment prefetched after last MFMA; store addresses loop-invariant with soffset SGPR
# baseline (speedup 1.0000x reference)
_Z12fused_kernelPKfS0_Pf:
	s_load_dwordx4 s[12:15], s[0:1], 0x0
	s_load_dwordx2 s[8:9], s[0:1], 0x10
	s_lshl_b32 s0, s2, 5
	s_and_b32 s0, s0, 0xe0
	s_lshr_b32 s3, s2, 3
	s_add_i32 s0, s0, s3
	v_and_b32_e32 v1, 63, v0
	v_lshrrev_b32_e32 v200, 6, v0
	s_lshl_b32 s0, s0, 17
	v_lshlrev_b32_e32 v194, 4, v0
	v_lshl_add_u32 v2, v200, 25, s0
	v_lshlrev_b32_e32 v198, 4, v1
	v_add_u32_e32 v106, 0x2000, v194
	v_add_u32_e32 v107, 0x4000, v194
	v_or_b32_e32 v203, v2, v198
	v_lshlrev_b32_e32 v196, 10, v200
	v_mov_b32_e32 v195, 0
	v_or_b32_e32 v233, v203, v196
	s_mov_b32 s7, 0x20000
	s_brev_b32 s6, 8
	s_waitcnt lgkmcnt(0)
	s_and_b32 s5, s13, 0xffff
	s_mov_b32 s4, s12
	buffer_load_dwordx4 v[70:73], v233, s[4:7], 0 offen nt
	v_or_b32_e32 v227, 0x2000, v233
	buffer_load_dwordx4 v[66:69], v227, s[4:7], 0 offen nt
	v_or_b32_e32 v226, 0x4000, v233
	buffer_load_dwordx4 v[78:81], v226, s[4:7], 0 offen nt
	v_or_b32_e32 v227, 0x6000, v233
	buffer_load_dwordx4 v[74:77], v227, s[4:7], 0 offen nt
	v_or_b32_e32 v226, 0x8000, v233
	buffer_load_dwordx4 v[86:89], v226, s[4:7], 0 offen nt
	v_or_b32_e32 v227, 0xa000, v233
	buffer_load_dwordx4 v[82:85], v227, s[4:7], 0 offen nt
	v_or_b32_e32 v226, 0xc000, v233
	buffer_load_dwordx4 v[94:97], v226, s[4:7], 0 offen nt
	v_or_b32_e32 v227, 0xe000, v233
	buffer_load_dwordx4 v[90:93], v227, s[4:7], 0 offen nt
	v_or_b32_e32 v226, 0x10000, v233
	buffer_load_dwordx4 v[150:153], v226, s[4:7], 0 offen nt
	v_or_b32_e32 v227, 0x12000, v233
	buffer_load_dwordx4 v[146:149], v227, s[4:7], 0 offen nt
	v_or_b32_e32 v226, 0x14000, v233
	buffer_load_dwordx4 v[162:165], v226, s[4:7], 0 offen nt
	v_or_b32_e32 v227, 0x16000, v233
	buffer_load_dwordx4 v[154:157], v227, s[4:7], 0 offen nt
	v_or_b32_e32 v226, 0x18000, v233
	buffer_load_dwordx4 v[174:177], v226, s[4:7], 0 offen nt
	v_or_b32_e32 v227, 0x1a000, v233
	buffer_load_dwordx4 v[166:169], v227, s[4:7], 0 offen nt
	v_or_b32_e32 v226, 0x1c000, v233
	buffer_load_dwordx4 v[182:185], v226, s[4:7], 0 offen nt
	v_or_b32_e32 v227, 0x1e000, v233
	buffer_load_dwordx4 v[178:181], v227, s[4:7], 0 offen nt
	global_load_dwordx4 v[228:231], v194, s[14:15]
	global_load_dwordx4 v[98:101], v106, s[14:15]
	global_load_dwordx4 v[102:105], v107, s[14:15]
	v_add_u32_e32 v107, 0x6000, v194
	global_load_dwordx4 v[116:119], v107, s[14:15]
	v_add_u32_e32 v106, 0x8000, v194
	global_load_dwordx4 v[120:123], v106, s[14:15]
	v_add_u32_e32 v107, 0xa000, v194
	global_load_dwordx4 v[124:127], v107, s[14:15]
	v_add_u32_e32 v106, 0xc000, v194
	global_load_dwordx4 v[128:131], v106, s[14:15]
	v_add_u32_e32 v107, 0xe000, v194
	global_load_dwordx4 v[132:135], v107, s[14:15]
	v_add_u32_e32 v106, 0x10000, v194
	global_load_dwordx4 v[136:139], v106, s[14:15]
	v_add_u32_e32 v107, 0x12000, v194
	global_load_dwordx4 v[140:143], v107, s[14:15]
	v_add_u32_e32 v106, 0x14000, v194
	global_load_dwordx4 v[158:161], v106, s[14:15]
	v_add_u32_e32 v107, 0x16000, v194
	global_load_dwordx4 v[170:173], v107, s[14:15]
	v_add_u32_e32 v106, 0x18000, v194
	global_load_dwordx4 v[186:189], v106, s[14:15]
	v_add_u32_e32 v107, 0x1a000, v194
	global_load_dwordx4 v[190:193], v107, s[14:15]
	v_add_u32_e32 v106, 0x1c000, v194
	global_load_dwordx4 v[204:207], v106, s[14:15]
	v_add_u32_e32 v107, 0x1e000, v194
	global_load_dwordx4 v[208:211], v107, s[14:15]
	v_add_u32_e32 v106, 0x20000, v194
	global_load_dwordx4 v[212:215], v106, s[14:15]
	v_add_u32_e32 v107, 0x22000, v194
	global_load_dwordx4 v[216:219], v107, s[14:15]
	v_add_u32_e32 v106, 0x24000, v194
	global_load_dwordx4 v[220:223], v106, s[14:15]
	v_add_u32_e32 v107, 0x26000, v194
	global_load_dwordx4 v[112:115], v107, s[14:15]
	v_add_u32_e32 v224, 0x400, v196
	s_movk_i32 s0, 0x1c00
	v_and_or_b32 v224, v224, s0, v203
	buffer_load_dwordx4 v[62:65], v224, s[4:7], 0 offen nt
	v_or_b32_e32 v227, 0x2000, v224
	buffer_load_dwordx4 v[38:41], v227, s[4:7], 0 offen nt
	v_or_b32_e32 v226, 0x4000, v224
	buffer_load_dwordx4 v[42:45], v226, s[4:7], 0 offen nt
	v_or_b32_e32 v227, 0x6000, v224
	buffer_load_dwordx4 v[14:17], v227, s[4:7], 0 offen nt
	v_or_b32_e32 v226, 0x8000, v224
	buffer_load_dwordx4 v[46:49], v226, s[4:7], 0 offen nt
	v_or_b32_e32 v227, 0xa000, v224
	buffer_load_dwordx4 v[18:21], v227, s[4:7], 0 offen nt
	v_or_b32_e32 v226, 0xc000, v224
	buffer_load_dwordx4 v[50:53], v226, s[4:7], 0 offen nt
	v_or_b32_e32 v227, 0xe000, v224
	buffer_load_dwordx4 v[22:25], v227, s[4:7], 0 offen nt
	v_or_b32_e32 v226, 0x10000, v224
	buffer_load_dwordx4 v[54:57], v226, s[4:7], 0 offen nt
	v_or_b32_e32 v227, 0x12000, v224
	buffer_load_dwordx4 v[26:29], v227, s[4:7], 0 offen nt
	v_or_b32_e32 v226, 0x14000, v224
	buffer_load_dwordx4 v[58:61], v226, s[4:7], 0 offen nt
	v_or_b32_e32 v227, 0x16000, v224
	buffer_load_dwordx4 v[30:33], v227, s[4:7], 0 offen nt
	v_or_b32_e32 v226, 0x18000, v224
	buffer_load_dwordx4 v[34:37], v226, s[4:7], 0 offen nt
	v_or_b32_e32 v227, 0x1a000, v224
	buffer_load_dwordx4 v[6:9], v227, s[4:7], 0 offen nt
	v_or_b32_e32 v226, 0x1c000, v224
	buffer_load_dwordx4 v[10:13], v226, s[4:7], 0 offen nt
	v_or_b32_e32 v227, 0x1e000, v224
	buffer_load_dwordx4 v[2:5], v227, s[4:7], 0 offen nt
	s_mov_b32 s1, 0xe000
	s_mov_b32 s10, 0xa000
	s_mov_b32 s11, 0x6000
	s_mov_b32 s12, 0xc000
	s_mov_b32 s13, 0x8000
	s_mov_b32 s14, 0x1e000
	s_mov_b32 s15, 0x1c000
	s_mov_b32 s16, 0x2000
	s_mov_b32 s17, 0x4000
	s_mov_b32 s18, 0x10000
	s_mov_b32 s19, 0x1a000
	s_mov_b32 s20, 0x18000
	s_mov_b32 s21, 0x16000
	s_mov_b32 s22, 0x14000
	s_mov_b32 s23, 0x12000
	s_mov_b32 s24, 0xe0
	s_mov_b32 s26, 0x3e13bb63
	v_lshrrev_b32_e32 v144, 3, v0
	v_bfe_u32 v145, v0, 1, 2
	v_lshlrev_b32_e32 v108, 3, v0
	v_and_b32_e32 v109, 8, v108
	v_lshlrev_b32_e32 v224, 8, v144
	v_lshlrev_b32_e32 v225, 6, v145
	v_lshlrev_b32_e32 v226, 8, v145
	v_lshlrev_b32_e32 v110, 10, v144
	v_or3_b32 v110, v226, v110, v109
	v_or3_b32 v111, v224, v225, v109
	v_add_u32_e32 v111, 0xff00, v111
	v_add_u32_e32 v144, 0x24800, v194
	v_bfe_u32 v201, v0, 4, 2
	v_and_b32_e32 v197, 15, v0
	v_lshlrev_b32_e32 v202, 2, v201
	s_waitcnt vmcnt(34)
	v_pk_add_f32 v[224:225], v[228:229], 0 op_sel_hi:[1,0]
	v_pk_add_f32 v[226:227], v[230:231], 0 op_sel_hi:[1,0]
	v_cvt_pk_bf16_f32 v228, v228, v229
	v_cvt_pk_bf16_f32 v229, v230, v231
	v_pk_add_f32 v[224:225], v[224:225], v[98:99]
	v_pk_add_f32 v[226:227], v[226:227], v[100:101]
	v_cvt_pk_bf16_f32 v98, v98, v99
	v_cvt_pk_bf16_f32 v99, v100, v101
	ds_write2_b64 v110, v[228:229], v[98:99] offset1:2
	s_waitcnt vmcnt(32)
	v_pk_add_f32 v[224:225], v[224:225], v[102:103]
	v_pk_add_f32 v[226:227], v[226:227], v[104:105]
	v_cvt_pk_bf16_f32 v102, v102, v103
	v_cvt_pk_bf16_f32 v103, v104, v105
	v_pk_add_f32 v[224:225], v[224:225], v[116:117]
	v_pk_add_f32 v[226:227], v[226:227], v[118:119]
	v_cvt_pk_bf16_f32 v116, v116, v117
	v_cvt_pk_bf16_f32 v117, v118, v119
	ds_write2_b64 v110, v[102:103], v[116:117] offset0:4 offset1:6
	s_waitcnt vmcnt(30)
	v_pk_add_f32 v[224:225], v[224:225], v[120:121]
	v_pk_add_f32 v[226:227], v[226:227], v[122:123]
	v_cvt_pk_bf16_f32 v120, v120, v121
	v_cvt_pk_bf16_f32 v121, v122, v123
	v_pk_add_f32 v[224:225], v[224:225], v[124:125]
	v_pk_add_f32 v[226:227], v[226:227], v[126:127]
	v_cvt_pk_bf16_f32 v124, v124, v125
	v_cvt_pk_bf16_f32 v125, v126, v127
	ds_write2_b64 v110, v[120:121], v[124:125] offset0:8 offset1:10
	s_waitcnt vmcnt(28)
	v_pk_add_f32 v[224:225], v[224:225], v[128:129]
	v_pk_add_f32 v[226:227], v[226:227], v[130:131]
	v_cvt_pk_bf16_f32 v128, v128, v129
	v_cvt_pk_bf16_f32 v129, v130, v131
	v_pk_add_f32 v[224:225], v[224:225], v[132:133]
	v_pk_add_f32 v[226:227], v[226:227], v[134:135]
	v_cvt_pk_bf16_f32 v132, v132, v133
	v_cvt_pk_bf16_f32 v133, v134, v135
	ds_write2_b64 v110, v[128:129], v[132:133] offset0:12 offset1:14
	s_waitcnt vmcnt(26)
	v_pk_add_f32 v[224:225], v[224:225], v[136:137]
	v_pk_add_f32 v[226:227], v[226:227], v[138:139]
	v_cvt_pk_bf16_f32 v136, v136, v137
	v_cvt_pk_bf16_f32 v137, v138, v139
	v_pk_add_f32 v[224:225], v[224:225], v[140:141]
	v_pk_add_f32 v[226:227], v[226:227], v[142:143]
	v_cvt_pk_bf16_f32 v140, v140, v141
	v_cvt_pk_bf16_f32 v141, v142, v143
	ds_write2_b64 v110, v[136:137], v[140:141] offset0:16 offset1:18
	s_waitcnt vmcnt(24)
	v_pk_add_f32 v[224:225], v[224:225], v[158:159]
	v_pk_add_f32 v[226:227], v[226:227], v[160:161]
	v_cvt_pk_bf16_f32 v158, v158, v159
	v_cvt_pk_bf16_f32 v159, v160, v161
	v_pk_add_f32 v[224:225], v[224:225], v[170:171]
	v_pk_add_f32 v[226:227], v[226:227], v[172:173]
	v_cvt_pk_bf16_f32 v170, v170, v171
	v_cvt_pk_bf16_f32 v171, v172, v173
	ds_write2_b64 v110, v[158:159], v[170:171] offset0:20 offset1:22
	s_waitcnt vmcnt(22)
	v_pk_add_f32 v[224:225], v[224:225], v[186:187]
	v_pk_add_f32 v[226:227], v[226:227], v[188:189]
	v_cvt_pk_bf16_f32 v186, v186, v187
	v_cvt_pk_bf16_f32 v187, v188, v189
	v_pk_add_f32 v[224:225], v[224:225], v[190:191]
	v_pk_add_f32 v[226:227], v[226:227], v[192:193]
	v_cvt_pk_bf16_f32 v190, v190, v191
	v_cvt_pk_bf16_f32 v191, v192, v193
	ds_write2_b64 v110, v[186:187], v[190:191] offset0:24 offset1:26
	s_waitcnt vmcnt(20)
	v_pk_add_f32 v[224:225], v[224:225], v[204:205]
	v_pk_add_f32 v[226:227], v[226:227], v[206:207]
	v_cvt_pk_bf16_f32 v204, v204, v205
	v_cvt_pk_bf16_f32 v205, v206, v207
	v_pk_add_f32 v[224:225], v[224:225], v[208:209]
	v_pk_add_f32 v[226:227], v[226:227], v[210:211]
	v_cvt_pk_bf16_f32 v208, v208, v209
	v_cvt_pk_bf16_f32 v209, v210, v211
	ds_write2_b64 v110, v[204:205], v[208:209] offset0:28 offset1:30
	s_waitcnt vmcnt(18)
	v_pk_add_f32 v[224:225], v[224:225], v[212:213]
	v_pk_add_f32 v[226:227], v[226:227], v[214:215]
	v_cvt_pk_bf16_f32 v212, v212, v213
	v_cvt_pk_bf16_f32 v213, v214, v215
	v_pk_add_f32 v[224:225], v[224:225], v[216:217]
	v_pk_add_f32 v[226:227], v[226:227], v[218:219]
	v_cvt_pk_bf16_f32 v216, v216, v217
	v_cvt_pk_bf16_f32 v217, v218, v219
	ds_write2_b64 v111, v[212:213], v[216:217] offset0:32 offset1:34
	s_waitcnt vmcnt(16)
	v_pk_add_f32 v[224:225], v[224:225], v[220:221]
	v_pk_add_f32 v[226:227], v[226:227], v[222:223]
	v_cvt_pk_bf16_f32 v220, v220, v221
	v_cvt_pk_bf16_f32 v221, v222, v223
	v_pk_add_f32 v[224:225], v[224:225], v[112:113]
	v_pk_add_f32 v[226:227], v[226:227], v[114:115]
	v_cvt_pk_bf16_f32 v112, v112, v113
	v_cvt_pk_bf16_f32 v113, v114, v115
	ds_write2_b64 v111, v[220:221], v[112:113] offset0:36 offset1:38
	v_pk_mul_f32 v[224:225], v[224:225], s[26:27] op_sel_hi:[1,0]
	v_pk_mul_f32 v[226:227], v[226:227], s[26:27] op_sel_hi:[1,0]
	ds_write_b128 v144, v[224:227]
	v_and_or_b32 v98, v0, 3, v202
	v_mov_b32_e32 v99, 0x10000
	v_lshl_or_b32 v204, v98, 4, v99
	s_movk_i32 s25, 0x2100
	v_mov_b32_e32 v98, 0x14000
	v_mad_u32_u24 v199, v200, s25, v98
	v_add_u32_e32 v98, 0x800, v196
	v_and_or_b32 v186, v98, s0, v203
	v_or_b32_e32 v98, 0x2000, v186
	s_waitcnt lgkmcnt(0)
	s_barrier
	buffer_load_dwordx4 v[102:105], v186, s[4:7], 0 offen nt
	s_nop 0
	buffer_load_dwordx4 v[98:101], v98, s[4:7], 0 offen nt
	v_or_b32_e32 v106, 0x4000, v186
	v_or_b32_e32 v107, 0x6000, v186
	v_or_b32_e32 v114, 0x8000, v186
	v_or_b32_e32 v115, 0xa000, v186
	v_or_b32_e32 v122, 0xc000, v186
	v_or_b32_e32 v123, 0xe000, v186
	v_or_b32_e32 v130, 0x10000, v186
	v_or_b32_e32 v131, 0x12000, v186
	v_or_b32_e32 v138, 0x14000, v186
	v_or_b32_e32 v139, 0x16000, v186
	v_or_b32_e32 v158, 0x18000, v186
	v_or_b32_e32 v159, 0x1a000, v186
	v_or_b32_e32 v187, 0x1c000, v186
	v_or_b32_e32 v186, 0x1e000, v186
	v_or_b32_e32 v213, v199, v109
	v_and_b32_e32 v214, 0x1f0, v108
	buffer_load_dwordx4 v[110:113], v106, s[4:7], 0 offen nt
	s_nop 0
	buffer_load_dwordx4 v[106:109], v107, s[4:7], 0 offen nt
	s_nop 0
	buffer_load_dwordx4 v[118:121], v114, s[4:7], 0 offen nt
	s_nop 0
	buffer_load_dwordx4 v[114:117], v115, s[4:7], 0 offen nt
	s_nop 0
	buffer_load_dwordx4 v[126:129], v122, s[4:7], 0 offen nt
	s_nop 0
	buffer_load_dwordx4 v[122:125], v123, s[4:7], 0 offen nt
	s_nop 0
	buffer_load_dwordx4 v[134:137], v130, s[4:7], 0 offen nt
	s_nop 0
	buffer_load_dwordx4 v[130:133], v131, s[4:7], 0 offen nt
	s_nop 0
	buffer_load_dwordx4 v[142:145], v138, s[4:7], 0 offen nt
	s_nop 0
	buffer_load_dwordx4 v[138:141], v139, s[4:7], 0 offen nt
	s_nop 0
	buffer_load_dwordx4 v[170:173], v158, s[4:7], 0 offen nt
	s_nop 0
	buffer_load_dwordx4 v[158:161], v159, s[4:7], 0 offen nt
	s_nop 0
	buffer_load_dwordx4 v[190:193], v187, s[4:7], 0 offen nt
	s_nop 0
	buffer_load_dwordx4 v[186:189], v186, s[4:7], 0 offen nt
	s_waitcnt vmcnt(32)
	v_cvt_pk_bf16_f32 v66, v66, v67
	v_cvt_pk_bf16_f32 v67, v68, v69
	s_movk_i32 s25, 0x50
	v_xad_u32 v207, v214, s25, v213
	s_movk_i32 s25, 0x60
	v_xad_u32 v206, v214, s25, v213
	s_movk_i32 s25, 0x70
	v_xad_u32 v205, v214, s25, v213
	s_movk_i32 s25, 0x80
	v_xad_u32 v211, v214, 16, v213
	v_xad_u32 v231, v214, s25, v213
	s_movk_i32 s25, 0x90
	v_xad_u32 v210, v214, 32, v213
	v_xad_u32 v230, v214, s25, v213
	s_movk_i32 s25, 0xa0
	ds_write_b64 v211, v[66:67] offset:512
	v_cvt_pk_bf16_f32 v66, v78, v79
	v_cvt_pk_bf16_f32 v67, v80, v81
	v_xad_u32 v209, v214, 48, v213
	v_xad_u32 v229, v214, s25, v213
	s_movk_i32 s25, 0xb0
	ds_write_b64 v210, v[66:67] offset:1024
	v_cvt_pk_bf16_f32 v66, v74, v75
	v_cvt_pk_bf16_f32 v67, v76, v77
	v_xad_u32 v208, v214, 64, v213
	v_xad_u32 v228, v214, s25, v213
	s_movk_i32 s25, 0xc0
	ds_write_b64 v209, v[66:67] offset:1536
	v_cvt_pk_bf16_f32 v66, v86, v87
	v_cvt_pk_bf16_f32 v67, v88, v89
	v_xad_u32 v227, v214, s25, v213
	s_movk_i32 s25, 0xd0
	v_xad_u32 v225, v214, s24, v213
	s_movk_i32 s24, 0xf0
	ds_write_b64 v208, v[66:67] offset:2048
	v_cvt_pk_bf16_f32 v66, v82, v83
	v_cvt_pk_bf16_f32 v67, v84, v85
	v_add_u32_e32 v212, v213, v214
	v_xad_u32 v226, v214, s25, v213
	v_xad_u32 v224, v214, s24, v213
	v_lshl_add_u32 v213, v197, 9, v199
	v_bitop3_b32 v214, v201, v0, 15 bitop3:0x78
	ds_write_b64 v207, v[66:67] offset:2560
	v_cvt_pk_bf16_f32 v66, v94, v95
	v_cvt_pk_bf16_f32 v67, v96, v97
	v_lshl_or_b32 v223, v214, 4, v213
	v_bitop3_b32 v214, v201, v197, 4 bitop3:0x36
	ds_write_b64 v206, v[66:67] offset:3072
	v_cvt_pk_bf16_f32 v66, v90, v91
	v_cvt_pk_bf16_f32 v67, v92, v93
	v_lshl_or_b32 v222, v214, 4, v213
	v_bitop3_b32 v214, v201, v197, 8 bitop3:0x36
	ds_write_b64 v205, v[66:67] offset:3584
	v_cvt_pk_bf16_f32 v66, v150, v151
	v_cvt_pk_bf16_f32 v67, v152, v153
	v_lshl_or_b32 v221, v214, 4, v213
	v_bitop3_b32 v214, v201, v197, 12 bitop3:0x36
	ds_write_b64 v231, v[66:67] offset:4096
	v_cvt_pk_bf16_f32 v66, v146, v147
	v_cvt_pk_bf16_f32 v67, v148, v149
	v_lshl_or_b32 v219, v214, 4, v213
	v_bitop3_b32 v214, v201, v197, 16 bitop3:0x36
	ds_write_b64 v230, v[66:67] offset:4608
	v_cvt_pk_bf16_f32 v66, v162, v163
	v_cvt_pk_bf16_f32 v67, v164, v165
	v_lshl_add_u32 v218, v214, 4, v213
	v_bitop3_b32 v214, v201, v197, 20 bitop3:0x36
	ds_write_b64 v229, v[66:67] offset:5120
	v_cvt_pk_bf16_f32 v66, v154, v155
	v_cvt_pk_bf16_f32 v67, v156, v157
	v_lshl_add_u32 v217, v214, 4, v213
	v_bitop3_b32 v214, v201, v197, 24 bitop3:0x36
	ds_write_b64 v228, v[66:67] offset:5632
	v_cvt_pk_bf16_f32 v66, v174, v175
	v_cvt_pk_bf16_f32 v67, v176, v177
	v_lshl_add_u32 v216, v214, 4, v213
	v_bitop3_b32 v214, v201, v197, 28 bitop3:0x36
	ds_write_b64 v227, v[66:67] offset:6144
	v_cvt_pk_bf16_f32 v66, v166, v167
	v_cvt_pk_bf16_f32 v67, v168, v169
	v_add_u32_e32 v235, 3, v200
	v_lshl_add_u32 v213, v214, 4, v213
	ds_write_b64 v226, v[66:67] offset:6656
	v_cvt_pk_bf16_f32 v66, v182, v183
	v_cvt_pk_bf16_f32 v67, v184, v185
	v_cvt_pk_bf16_f32 v70, v70, v71
	v_cvt_pk_bf16_f32 v71, v72, v73
	ds_write_b64 v212, v[70:71]
	ds_write_b64 v225, v[66:67] offset:7168
	v_cvt_pk_bf16_f32 v66, v178, v179
	v_cvt_pk_bf16_f32 v67, v180, v181
	ds_write_b64 v224, v[66:67] offset:7680
	v_lshl_or_b32 v66, v200, 13, v198
	ds_read_b128 v[66:69], v66
	v_lshlrev_b32_e32 v220, 11, v200
	v_or_b32_e32 v70, v204, v220
	ds_read_b128 v[70:73], v70
	ds_read_b128 v[74:77], v223
	v_lshlrev_b32_e32 v232, 3, v200
	v_or_b32_e32 v214, 1, v232
	s_waitcnt lgkmcnt(0)
	v_mfma_f32_16x16x32_bf16 v[70:73], v[70:73], v[74:77], 0
	v_lshlrev_b32_e32 v215, 8, v214
	v_or_b32_e32 v78, v204, v215
	v_or_b32_e32 v184, 2, v232
	v_mfma_f32_16x16x32_bf16 v[66:69], v[66:69], v[74:77], 0
	v_lshl_or_b32 v74, v214, 10, v198
	ds_read_b128 v[74:77], v74
	ds_read_b128 v[78:81], v78
	ds_read_b128 v[82:85], v222
	v_lshlrev_b32_e32 v185, 8, v184
	s_waitcnt lgkmcnt(0)
	v_mfma_f32_16x16x32_bf16 v[70:73], v[78:81], v[82:85], v[70:73]
	v_or_b32_e32 v78, v204, v185
	v_or_b32_e32 v182, 3, v232
	v_lshlrev_b32_e32 v183, 8, v182
	v_mfma_f32_16x16x32_bf16 v[66:69], v[74:77], v[82:85], v[66:69]
	v_lshl_or_b32 v74, v184, 10, v198
	ds_read_b128 v[74:77], v74
	ds_read_b128 v[78:81], v78
	ds_read_b128 v[82:85], v221
	s_waitcnt lgkmcnt(0)
	v_mfma_f32_16x16x32_bf16 v[70:73], v[78:81], v[82:85], v[70:73]
	v_or_b32_e32 v78, v204, v183
	v_or_b32_e32 v180, 4, v232
	v_lshlrev_b32_e32 v181, 8, v180
	v_mfma_f32_16x16x32_bf16 v[66:69], v[74:77], v[82:85], v[66:69]
	v_lshl_or_b32 v74, v182, 10, v198
	ds_read_b128 v[74:77], v74
	ds_read_b128 v[78:81], v78
	ds_read_b128 v[82:85], v219
	s_waitcnt lgkmcnt(0)
	v_mfma_f32_16x16x32_bf16 v[66:69], v[74:77], v[82:85], v[66:69]
	v_lshl_or_b32 v74, v180, 10, v198
	ds_read_b128 v[74:77], v74
	v_or_b32_e32 v178, 5, v232
	v_mfma_f32_16x16x32_bf16 v[70:73], v[78:81], v[82:85], v[70:73]
	v_or_b32_e32 v78, v204, v181
	ds_read_b128 v[78:81], v78
	ds_read_b128 v[82:85], v218
	v_lshlrev_b32_e32 v179, 8, v178
	s_waitcnt lgkmcnt(0)
	v_mfma_f32_16x16x32_bf16 v[66:69], v[74:77], v[82:85], v[66:69]
	v_lshl_or_b32 v74, v178, 10, v198
	ds_read_b128 v[74:77], v74
	v_or_b32_e32 v176, 6, v232
	v_mfma_f32_16x16x32_bf16 v[70:73], v[78:81], v[82:85], v[70:73]
	v_or_b32_e32 v78, v204, v179
	ds_read_b128 v[78:81], v78
	ds_read_b128 v[82:85], v217
	v_lshlrev_b32_e32 v177, 8, v176
	s_waitcnt lgkmcnt(0)
	v_mfma_f32_16x16x32_bf16 v[66:69], v[74:77], v[82:85], v[66:69]
	v_lshl_or_b32 v74, v176, 10, v198
	ds_read_b128 v[74:77], v74
	v_or_b32_e32 v174, 7, v232
	v_mfma_f32_16x16x32_bf16 v[70:73], v[78:81], v[82:85], v[70:73]
	v_or_b32_e32 v78, v204, v177
	ds_read_b128 v[78:81], v78
	ds_read_b128 v[82:85], v216
	v_lshlrev_b32_e32 v175, 8, v174
	s_waitcnt lgkmcnt(0)
	v_mfma_f32_16x16x32_bf16 v[66:69], v[74:77], v[82:85], v[66:69]
	v_lshl_or_b32 v74, v174, 10, v198
	s_waitcnt vmcnt(16)
	v_cvt_pk_bf16_f32 v14, v14, v15
	v_cvt_pk_bf16_f32 v15, v16, v17
	v_mfma_f32_16x16x32_bf16 v[70:73], v[78:81], v[82:85], v[70:73]
	v_or_b32_e32 v78, v204, v175
	ds_read_b128 v[74:77], v74
	ds_read_b128 v[78:81], v78
	ds_read_b128 v[82:85], v213
	ds_write_b64 v209, v[14:15] offset:1536
	v_cvt_pk_bf16_f32 v14, v46, v47
	v_cvt_pk_bf16_f32 v15, v48, v49
	ds_write_b64 v208, v[14:15] offset:2048
	v_cvt_pk_bf16_f32 v14, v18, v19
	v_cvt_pk_bf16_f32 v15, v20, v21
	ds_write_b64 v207, v[14:15] offset:2560
	v_cvt_pk_bf16_f32 v14, v50, v51
	v_cvt_pk_bf16_f32 v15, v52, v53
	ds_write_b64 v206, v[14:15] offset:3072
	v_cvt_pk_bf16_f32 v14, v22, v23
	v_cvt_pk_bf16_f32 v15, v24, v25
	ds_write_b64 v205, v[14:15] offset:3584
	v_cvt_pk_bf16_f32 v14, v54, v55
	v_cvt_pk_bf16_f32 v15, v56, v57
	v_cvt_pk_bf16_f32 v6, v6, v7
	v_cvt_pk_bf16_f32 v2, v2, v3
	ds_write_b64 v231, v[14:15] offset:4096
	v_cvt_pk_bf16_f32 v14, v26, v27
	v_cvt_pk_bf16_f32 v15, v28, v29
	v_cvt_pk_bf16_f32 v7, v8, v9
	ds_write_b64 v226, v[6:7] offset:6656
	v_cvt_pk_bf16_f32 v6, v10, v11
	v_cvt_pk_bf16_f32 v3, v4, v5
	ds_write_b64 v224, v[2:3] offset:7680
	v_lshlrev_b32_e32 v2, 10, v235
	ds_write_b64 v230, v[14:15] offset:4608
	v_cvt_pk_bf16_f32 v14, v58, v59
	v_cvt_pk_bf16_f32 v15, v60, v61
	v_cvt_pk_bf16_f32 v7, v12, v13
	ds_write_b64 v225, v[6:7] offset:7168
	v_and_or_b32 v6, v2, s0, v203
	ds_write_b64 v229, v[14:15] offset:5120
	v_cvt_pk_bf16_f32 v14, v30, v31
	v_cvt_pk_bf16_f32 v15, v32, v33
	v_or_b32_e32 v7, 0x2000, v6
	ds_write_b64 v228, v[14:15] offset:5632
	v_cvt_pk_bf16_f32 v14, v34, v35
	v_cvt_pk_bf16_f32 v15, v36, v37
	buffer_load_dwordx4 v[2:5], v6, s[4:7], 0 offen nt
	buffer_load_dwordx4 v[10:13], v7, s[4:7], 0 offen nt
	v_or_b32_e32 v7, 0x4000, v6
	ds_write_b64 v227, v[14:15] offset:6144
	buffer_load_dwordx4 v[14:17], v7, s[4:7], 0 offen nt
	v_or_b32_e32 v7, 0x6000, v6
	v_cvt_pk_bf16_f32 v38, v38, v39
	v_cvt_pk_bf16_f32 v39, v40, v41
	buffer_load_dwordx4 v[22:25], v7, s[4:7], 0 offen nt
	v_or_b32_e32 v7, 0x8000, v6
	ds_write_b64 v211, v[38:39] offset:512
	v_cvt_pk_bf16_f32 v38, v42, v43
	v_cvt_pk_bf16_f32 v39, v44, v45
	buffer_load_dwordx4 v[30:33], v7, s[4:7], 0 offen nt
	v_or_b32_e32 v7, 0xa000, v6
	ds_write_b64 v210, v[38:39] offset:1024
	buffer_load_dwordx4 v[38:41], v7, s[4:7], 0 offen nt
	v_or_b32_e32 v7, 0xc000, v6
	buffer_load_dwordx4 v[46:49], v7, s[4:7], 0 offen nt
	v_or_b32_e32 v7, 0xe000, v6
	v_cvt_pk_bf16_f32 v62, v62, v63
	v_cvt_pk_bf16_f32 v63, v64, v65
	buffer_load_dwordx4 v[54:57], v7, s[4:7], 0 offen nt
	v_or_b32_e32 v7, 0x10000, v6
	ds_write_b64 v212, v[62:63]
	buffer_load_dwordx4 v[62:65], v7, s[4:7], 0 offen nt
	v_or_b32_e32 v7, 0x12000, v6
	s_waitcnt lgkmcnt(14)
	v_mfma_f32_16x16x32_bf16 v[66:69], v[74:77], v[82:85], v[66:69]
	v_mfma_f32_16x16x32_bf16 v[74:77], v[78:81], v[82:85], v[70:73]
	s_nop 2
	buffer_load_dwordx4 v[70:73], v7, s[4:7], 0 offen nt
	v_or_b32_e32 v7, 0x14000, v6
	buffer_load_dwordx4 v[78:81], v7, s[4:7], 0 offen nt
	v_or_b32_e32 v7, 0x16000, v6
	buffer_load_dwordx4 v[86:89], v7, s[4:7], 0 offen nt
	v_or_b32_e32 v7, 0x18000, v6
	buffer_load_dwordx4 v[94:97], v7, s[4:7], 0 offen nt
	v_or_b32_e32 v7, 0x1a000, v6
	buffer_load_dwordx4 v[146:149], v7, s[4:7], 0 offen nt
	v_or_b32_e32 v7, 0x1c000, v6
	v_or_b32_e32 v6, 0x1e000, v6
	buffer_load_dwordx4 v[150:153], v7, s[4:7], 0 offen nt
	buffer_load_dwordx4 v[154:157], v6, s[4:7], 0 offen nt
	v_add_u32_e32 v6, 8, v232
	v_and_b32_e32 v50, 56, v6
	v_lshl_or_b32 v6, v50, 10, v198
	ds_read_b128 v[6:9], v6
	v_lshl_or_b32 v18, v50, 8, v204
	ds_read_b128 v[18:21], v18
	ds_read_b128 v[26:29], v223
	v_or_b32_e32 v34, 1, v50
	s_movk_i32 s24, 0x1000
	s_waitcnt lgkmcnt(0)
	v_mfma_f32_16x16x32_bf16 v[18:21], v[18:21], v[26:29], v[74:77]
	v_add_u32_e32 v234, 5, v200
	v_mfma_f32_16x16x32_bf16 v[6:9], v[6:9], v[26:29], v[66:69]
	v_lshl_or_b32 v26, v34, 10, v198
	ds_read_b128 v[26:29], v26
	v_lshl_or_b32 v34, v34, 8, v204
	ds_read_b128 v[34:37], v34
	ds_read_b128 v[42:45], v222
	s_waitcnt lgkmcnt(0)
	v_mfma_f32_16x16x32_bf16 v[18:21], v[34:37], v[42:45], v[18:21]
	v_or_b32_e32 v34, 2, v50
	v_mfma_f32_16x16x32_bf16 v[6:9], v[26:29], v[42:45], v[6:9]
	v_lshl_or_b32 v26, v34, 10, v198
	ds_read_b128 v[26:29], v26
	v_lshl_or_b32 v34, v34, 8, v204
	ds_read_b128 v[34:37], v34
	ds_read_b128 v[42:45], v221
	s_waitcnt lgkmcnt(0)
	v_mfma_f32_16x16x32_bf16 v[18:21], v[34:37], v[42:45], v[18:21]
	v_or_b32_e32 v34, 3, v50
	v_mfma_f32_16x16x32_bf16 v[6:9], v[26:29], v[42:45], v[6:9]
	v_lshl_or_b32 v26, v34, 10, v198
	ds_read_b128 v[26:29], v26
	v_lshl_or_b32 v34, v34, 8, v204
	ds_read_b128 v[34:37], v34
	ds_read_b128 v[42:45], v219
	s_waitcnt lgkmcnt(0)
	v_mfma_f32_16x16x32_bf16 v[18:21], v[34:37], v[42:45], v[18:21]
	v_or_b32_e32 v34, 4, v50
	v_mfma_f32_16x16x32_bf16 v[6:9], v[26:29], v[42:45], v[6:9]
	v_lshl_or_b32 v26, v34, 10, v198
	ds_read_b128 v[26:29], v26
	v_lshl_or_b32 v34, v34, 8, v204
	ds_read_b128 v[34:37], v34
	ds_read_b128 v[42:45], v218
	s_waitcnt lgkmcnt(0)
	v_mfma_f32_16x16x32_bf16 v[18:21], v[34:37], v[42:45], v[18:21]
	v_or_b32_e32 v34, 5, v50
	v_mfma_f32_16x16x32_bf16 v[6:9], v[26:29], v[42:45], v[6:9]
	v_lshl_or_b32 v26, v34, 10, v198
	ds_read_b128 v[26:29], v26
	v_lshl_or_b32 v34, v34, 8, v204
	ds_read_b128 v[34:37], v34
	ds_read_b128 v[42:45], v217
	s_waitcnt lgkmcnt(0)
	v_mfma_f32_16x16x32_bf16 v[18:21], v[34:37], v[42:45], v[18:21]
	v_or_b32_e32 v34, 6, v50
	v_mfma_f32_16x16x32_bf16 v[6:9], v[26:29], v[42:45], v[6:9]
	v_lshl_or_b32 v26, v34, 10, v198
	ds_read_b128 v[26:29], v26
	v_lshl_or_b32 v34, v34, 8, v204
	ds_read_b128 v[34:37], v34
	ds_read_b128 v[42:45], v216
	s_waitcnt lgkmcnt(0)
	v_mfma_f32_16x16x32_bf16 v[18:21], v[34:37], v[42:45], v[18:21]
	v_or_b32_e32 v34, 7, v50
	v_mfma_f32_16x16x32_bf16 v[6:9], v[26:29], v[42:45], v[6:9]
	v_lshl_or_b32 v26, v34, 10, v198
	ds_read_b128 v[26:29], v26
	v_lshl_or_b32 v34, v34, 8, v204
	ds_read_b128 v[34:37], v34
	ds_read_b128 v[42:45], v213
	s_waitcnt lgkmcnt(0)
	v_mfma_f32_16x16x32_bf16 v[162:165], v[26:29], v[42:45], v[6:9]
	s_waitcnt vmcnt(31)
	s_nop 1
	v_cvt_pk_bf16_f32 v6, v102, v103
	v_cvt_pk_bf16_f32 v7, v104, v105
	ds_write_b64 v212, v[6:7]
	s_waitcnt vmcnt(30)
	v_cvt_pk_bf16_f32 v6, v98, v99
	v_cvt_pk_bf16_f32 v7, v100, v101
	ds_write_b64 v211, v[6:7] offset:512
	s_waitcnt vmcnt(29)
	v_cvt_pk_bf16_f32 v6, v110, v111
	v_cvt_pk_bf16_f32 v7, v112, v113
	ds_write_b64 v210, v[6:7] offset:1024
	s_waitcnt vmcnt(28)
	v_cvt_pk_bf16_f32 v6, v106, v107
	v_cvt_pk_bf16_f32 v7, v108, v109
	ds_write_b64 v209, v[6:7] offset:1536
	s_waitcnt vmcnt(27)
	v_cvt_pk_bf16_f32 v6, v118, v119
	v_cvt_pk_bf16_f32 v7, v120, v121
	ds_write_b64 v208, v[6:7] offset:2048
	s_waitcnt vmcnt(26)
	v_cvt_pk_bf16_f32 v6, v114, v115
	v_cvt_pk_bf16_f32 v7, v116, v117
	ds_write_b64 v207, v[6:7] offset:2560
	s_waitcnt vmcnt(25)
	v_cvt_pk_bf16_f32 v6, v126, v127
	v_cvt_pk_bf16_f32 v7, v128, v129
	ds_write_b64 v206, v[6:7] offset:3072
	s_waitcnt vmcnt(24)
	v_cvt_pk_bf16_f32 v6, v122, v123
	v_cvt_pk_bf16_f32 v7, v124, v125
	ds_write_b64 v205, v[6:7] offset:3584
	s_waitcnt vmcnt(23)
	v_cvt_pk_bf16_f32 v6, v134, v135
	v_cvt_pk_bf16_f32 v7, v136, v137
	ds_write_b64 v231, v[6:7] offset:4096
	s_waitcnt vmcnt(22)
	v_cvt_pk_bf16_f32 v6, v130, v131
	v_cvt_pk_bf16_f32 v7, v132, v133
	ds_write_b64 v230, v[6:7] offset:4608
	s_waitcnt vmcnt(21)
	v_cvt_pk_bf16_f32 v6, v142, v143
	v_cvt_pk_bf16_f32 v7, v144, v145
	ds_write_b64 v229, v[6:7] offset:5120
	s_waitcnt vmcnt(20)
	v_cvt_pk_bf16_f32 v6, v138, v139
	v_cvt_pk_bf16_f32 v7, v140, v141
	ds_write_b64 v228, v[6:7] offset:5632
	s_waitcnt vmcnt(19)
	v_cvt_pk_bf16_f32 v6, v170, v171
	v_cvt_pk_bf16_f32 v7, v172, v173
	ds_write_b64 v227, v[6:7] offset:6144
	s_waitcnt vmcnt(18)
	v_cvt_pk_bf16_f32 v6, v158, v159
	v_mov_b32_e32 v106, 0x1000
	v_cvt_pk_bf16_f32 v7, v160, v161
	ds_write_b64 v226, v[6:7] offset:6656
	s_waitcnt vmcnt(17)
	v_cvt_pk_bf16_f32 v6, v190, v191
	v_bitop3_b32 v107, v233, s19, v106 bitop3:0xde
	v_mfma_f32_16x16x32_bf16 v[166:169], v[34:37], v[42:45], v[18:21]
	v_cvt_pk_bf16_f32 v7, v192, v193
	ds_write_b64 v225, v[6:7] offset:7168
	s_waitcnt vmcnt(16)
	v_cvt_pk_bf16_f32 v6, v186, v187
	v_bitop3_b32 v26, v233, s17, v106 bitop3:0xde
	v_bitop3_b32 v34, v233, s11, v106 bitop3:0xde
	v_bitop3_b32 v18, v233, s16, v106 bitop3:0xde
	v_bitop3_b32 v42, v233, s13, v106 bitop3:0xde
	v_bitop3_b32 v50, v233, s10, v106 bitop3:0xde
	v_bitop3_b32 v58, v233, s12, v106 bitop3:0xde
	v_bitop3_b32 v66, v233, s1, v106 bitop3:0xde
	v_bitop3_b32 v74, v233, s18, v106 bitop3:0xde
	v_bitop3_b32 v82, v233, s23, v106 bitop3:0xde
	v_bitop3_b32 v90, v233, s22, v106 bitop3:0xde
	v_bitop3_b32 v98, v233, s21, v106 bitop3:0xde
	v_bitop3_b32 v102, v233, s20, v106 bitop3:0xde
	buffer_load_dwordx4 v[110:113], v107, s[4:7], 0 offen nt
	v_bitop3_b32 v107, v233, s15, v106 bitop3:0xde
	v_bitop3_b32 v106, v233, s14, v106 bitop3:0xde
	v_cvt_pk_bf16_f32 v7, v188, v189
	ds_write_b64 v224, v[6:7] offset:7680
	v_bitop3_b32 v6, v203, s24, v196 bitop3:0x36
	buffer_load_dwordx4 v[42:45], v42, s[4:7], 0 offen nt
	s_nop 0
	buffer_load_dwordx4 v[50:53], v50, s[4:7], 0 offen nt
	s_nop 0
	buffer_load_dwordx4 v[58:61], v58, s[4:7], 0 offen nt
	s_nop 0
	buffer_load_dwordx4 v[66:69], v66, s[4:7], 0 offen nt
	s_nop 0
	buffer_load_dwordx4 v[74:77], v74, s[4:7], 0 offen nt
	s_nop 0
	buffer_load_dwordx4 v[82:85], v82, s[4:7], 0 offen nt
	s_nop 0
	buffer_load_dwordx4 v[90:93], v90, s[4:7], 0 offen nt
	s_nop 0
	buffer_load_dwordx4 v[98:101], v98, s[4:7], 0 offen nt
	s_nop 0
	buffer_load_dwordx4 v[102:105], v102, s[4:7], 0 offen nt
	s_nop 0
	buffer_load_dwordx4 v[126:129], v106, s[4:7], 0 offen nt
	buffer_load_dwordx4 v[118:121], v107, s[4:7], 0 offen nt
	s_nop 0
	buffer_load_dwordx4 v[6:9], v6, s[4:7], 0 offen nt
	s_nop 0
	buffer_load_dwordx4 v[18:21], v18, s[4:7], 0 offen nt
	s_nop 0
	buffer_load_dwordx4 v[26:29], v26, s[4:7], 0 offen nt
	s_nop 0
	buffer_load_dwordx4 v[34:37], v34, s[4:7], 0 offen nt
	v_add_u32_e32 v106, 16, v232
	v_and_b32_e32 v138, 56, v106
	v_lshl_or_b32 v106, v138, 10, v198
	ds_read_b128 v[106:109], v106
	v_lshl_or_b32 v114, v138, 8, v204
	ds_read_b128 v[114:117], v114
	ds_read_b128 v[122:125], v223
	v_or_b32_e32 v130, 1, v138
	s_waitcnt vmcnt(31)
	v_cvt_pk_bf16_f32 v2, v2, v3
	s_waitcnt lgkmcnt(0)
	v_mfma_f32_16x16x32_bf16 v[114:117], v[114:117], v[122:125], v[166:169]
	v_cvt_pk_bf16_f32 v3, v4, v5
	v_mfma_f32_16x16x32_bf16 v[106:109], v[106:109], v[122:125], v[162:165]
	v_lshl_or_b32 v122, v130, 10, v198
	ds_read_b128 v[122:125], v122
	v_lshl_or_b32 v130, v130, 8, v204
	ds_read_b128 v[130:133], v130
	ds_read_b128 v[134:137], v222
	s_waitcnt lgkmcnt(0)
	v_mfma_f32_16x16x32_bf16 v[114:117], v[130:133], v[134:137], v[114:117]
	v_or_b32_e32 v130, 2, v138
	v_mfma_f32_16x16x32_bf16 v[106:109], v[122:125], v[134:137], v[106:109]
	v_lshl_or_b32 v122, v130, 10, v198
	ds_read_b128 v[122:125], v122
	v_lshl_or_b32 v130, v130, 8, v204
	ds_read_b128 v[130:133], v130
	ds_read_b128 v[134:137], v221
	s_waitcnt lgkmcnt(0)
	v_mfma_f32_16x16x32_bf16 v[114:117], v[130:133], v[134:137], v[114:117]
	v_or_b32_e32 v130, 3, v138
	v_mfma_f32_16x16x32_bf16 v[106:109], v[122:125], v[134:137], v[106:109]
	v_lshl_or_b32 v122, v130, 10, v198
	ds_read_b128 v[122:125], v122
	v_lshl_or_b32 v130, v130, 8, v204
	ds_read_b128 v[130:133], v130
	ds_read_b128 v[134:137], v219
	s_waitcnt lgkmcnt(0)
	v_mfma_f32_16x16x32_bf16 v[114:117], v[130:133], v[134:137], v[114:117]
	v_or_b32_e32 v130, 4, v138
	v_mfma_f32_16x16x32_bf16 v[106:109], v[122:125], v[134:137], v[106:109]
	v_lshl_or_b32 v122, v130, 10, v198
	ds_read_b128 v[122:125], v122
	v_lshl_or_b32 v130, v130, 8, v204
	ds_read_b128 v[130:133], v130
	ds_read_b128 v[134:137], v218
	s_waitcnt lgkmcnt(0)
	v_mfma_f32_16x16x32_bf16 v[114:117], v[130:133], v[134:137], v[114:117]
	v_or_b32_e32 v130, 5, v138
	v_mfma_f32_16x16x32_bf16 v[106:109], v[122:125], v[134:137], v[106:109]
	v_lshl_or_b32 v122, v130, 10, v198
	ds_read_b128 v[122:125], v122
	v_lshl_or_b32 v130, v130, 8, v204
	ds_read_b128 v[130:133], v130
	ds_read_b128 v[134:137], v217
	s_waitcnt lgkmcnt(0)
	v_mfma_f32_16x16x32_bf16 v[114:117], v[130:133], v[134:137], v[114:117]
	v_or_b32_e32 v130, 6, v138
	v_mfma_f32_16x16x32_bf16 v[106:109], v[122:125], v[134:137], v[106:109]
	v_lshl_or_b32 v122, v130, 10, v198
	ds_read_b128 v[122:125], v122
	v_lshl_or_b32 v130, v130, 8, v204
	ds_read_b128 v[130:133], v130
	ds_read_b128 v[134:137], v216
	s_waitcnt lgkmcnt(0)
	v_mfma_f32_16x16x32_bf16 v[114:117], v[130:133], v[134:137], v[114:117]
	v_or_b32_e32 v130, 7, v138
	v_mfma_f32_16x16x32_bf16 v[106:109], v[122:125], v[134:137], v[106:109]
	v_lshl_or_b32 v122, v130, 10, v198
	v_lshl_or_b32 v130, v130, 8, v204
	ds_read_b128 v[122:125], v122
	ds_read_b128 v[134:137], v130
	ds_read_b128 v[138:141], v213
	ds_write_b64 v212, v[2:3]
	s_waitcnt vmcnt(30)
	v_cvt_pk_bf16_f32 v2, v10, v11
	v_cvt_pk_bf16_f32 v3, v12, v13
	ds_write_b64 v211, v[2:3] offset:512
	s_waitcnt vmcnt(29)
	v_cvt_pk_bf16_f32 v2, v14, v15
	v_cvt_pk_bf16_f32 v3, v16, v17
	ds_write_b64 v210, v[2:3] offset:1024
	s_waitcnt vmcnt(28)
	v_cvt_pk_bf16_f32 v2, v22, v23
	v_cvt_pk_bf16_f32 v3, v24, v25
	ds_write_b64 v209, v[2:3] offset:1536
	s_waitcnt vmcnt(27)
	v_cvt_pk_bf16_f32 v2, v30, v31
	v_cvt_pk_bf16_f32 v3, v32, v33
	ds_write_b64 v208, v[2:3] offset:2048
	s_waitcnt vmcnt(26)
	v_cvt_pk_bf16_f32 v2, v38, v39
	v_cvt_pk_bf16_f32 v3, v40, v41
	ds_write_b64 v207, v[2:3] offset:2560
	s_waitcnt vmcnt(25)
	v_cvt_pk_bf16_f32 v2, v46, v47
	v_cvt_pk_bf16_f32 v3, v48, v49
	ds_write_b64 v206, v[2:3] offset:3072
	s_waitcnt vmcnt(24)
	v_cvt_pk_bf16_f32 v2, v54, v55
	v_cvt_pk_bf16_f32 v3, v56, v57
	ds_write_b64 v205, v[2:3] offset:3584
	s_waitcnt vmcnt(23)
	v_cvt_pk_bf16_f32 v2, v62, v63
	v_cvt_pk_bf16_f32 v3, v64, v65
	ds_write_b64 v231, v[2:3] offset:4096
	s_waitcnt vmcnt(22)
	v_cvt_pk_bf16_f32 v2, v70, v71
	v_cvt_pk_bf16_f32 v3, v72, v73
	ds_write_b64 v230, v[2:3] offset:4608
	s_waitcnt vmcnt(21)
	v_cvt_pk_bf16_f32 v2, v78, v79
	v_cvt_pk_bf16_f32 v3, v80, v81
	ds_write_b64 v229, v[2:3] offset:5120
	s_waitcnt vmcnt(20)
	v_cvt_pk_bf16_f32 v2, v86, v87
	v_cvt_pk_bf16_f32 v3, v88, v89
	ds_write_b64 v228, v[2:3] offset:5632
	s_waitcnt vmcnt(19)
	v_cvt_pk_bf16_f32 v2, v94, v95
	v_cvt_pk_bf16_f32 v3, v96, v97
	ds_write_b64 v227, v[2:3] offset:6144
	s_waitcnt vmcnt(18)
	v_cvt_pk_bf16_f32 v2, v146, v147
	v_cvt_pk_bf16_f32 v3, v148, v149
	ds_write_b64 v226, v[2:3] offset:6656
	s_waitcnt vmcnt(17)
	v_cvt_pk_bf16_f32 v2, v150, v151
	v_cvt_pk_bf16_f32 v3, v152, v153
	ds_write_b64 v225, v[2:3] offset:7168
	s_waitcnt vmcnt(16)
	v_cvt_pk_bf16_f32 v2, v154, v155
	v_cvt_pk_bf16_f32 v3, v156, v157
	ds_write_b64 v224, v[2:3] offset:7680
	v_lshlrev_b32_e32 v2, 10, v234
	s_waitcnt lgkmcnt(14)
	v_mfma_f32_16x16x32_bf16 v[130:133], v[122:125], v[138:141], v[106:109]
	v_and_or_b32 v122, v2, s0, v203
	buffer_load_dwordx4 v[2:5], v122, s[4:7], 0 offen nt
	v_or_b32_e32 v10, 0x2000, v122
	v_mfma_f32_16x16x32_bf16 v[134:137], v[134:137], v[138:141], v[114:117]
	v_or_b32_e32 v14, 0x4000, v122
	v_or_b32_e32 v22, 0x6000, v122
	v_or_b32_e32 v30, 0x8000, v122
	v_or_b32_e32 v38, 0xa000, v122
	v_or_b32_e32 v46, 0xc000, v122
	v_or_b32_e32 v54, 0xe000, v122
	v_or_b32_e32 v62, 0x10000, v122
	v_or_b32_e32 v70, 0x12000, v122
	v_or_b32_e32 v78, 0x14000, v122
	v_or_b32_e32 v86, 0x16000, v122
	v_or_b32_e32 v94, 0x18000, v122
	v_or_b32_e32 v106, 0x1a000, v122
	v_or_b32_e32 v114, 0x1c000, v122
	v_or_b32_e32 v122, 0x1e000, v122
	buffer_load_dwordx4 v[54:57], v54, s[4:7], 0 offen nt
	s_nop 0
	buffer_load_dwordx4 v[62:65], v62, s[4:7], 0 offen nt
	s_nop 0
	buffer_load_dwordx4 v[70:73], v70, s[4:7], 0 offen nt
	s_nop 0
	buffer_load_dwordx4 v[78:81], v78, s[4:7], 0 offen nt
	s_nop 0
	buffer_load_dwordx4 v[86:89], v86, s[4:7], 0 offen nt
	s_nop 0
	buffer_load_dwordx4 v[94:97], v94, s[4:7], 0 offen nt
	s_nop 0
	buffer_load_dwordx4 v[106:109], v106, s[4:7], 0 offen nt
	s_nop 0
	buffer_load_dwordx4 v[114:117], v114, s[4:7], 0 offen nt
	s_nop 0
	buffer_load_dwordx4 v[122:125], v122, s[4:7], 0 offen nt
	s_nop 0
	buffer_load_dwordx4 v[10:13], v10, s[4:7], 0 offen nt
	s_nop 0
	buffer_load_dwordx4 v[14:17], v14, s[4:7], 0 offen nt
	s_nop 0
	buffer_load_dwordx4 v[22:25], v22, s[4:7], 0 offen nt
	s_nop 0
	buffer_load_dwordx4 v[30:33], v30, s[4:7], 0 offen nt
	s_nop 0
	buffer_load_dwordx4 v[38:41], v38, s[4:7], 0 offen nt
	s_nop 0
	buffer_load_dwordx4 v[46:49], v46, s[4:7], 0 offen nt
	v_lshlrev_b32_e32 v138, 3, v235
	v_and_b32_e32 v150, 56, v138
	v_lshl_or_b32 v138, v150, 10, v198
	ds_read_b128 v[138:141], v138
	v_lshl_or_b32 v142, v150, 8, v204
	ds_read_b128 v[142:145], v142
	ds_read_b128 v[146:149], v223
	s_waitcnt vmcnt(19)
	v_cvt_pk_bf16_f32 v6, v6, v7
	v_cvt_pk_bf16_f32 v7, v8, v9
	s_waitcnt lgkmcnt(0)
	v_mfma_f32_16x16x32_bf16 v[134:137], v[142:145], v[146:149], v[134:137]
	v_or_b32_e32 v142, 1, v150
	v_mfma_f32_16x16x32_bf16 v[130:133], v[138:141], v[146:149], v[130:133]
	v_lshl_or_b32 v138, v142, 10, v198
	ds_read_b128 v[138:141], v138
	v_lshl_or_b32 v142, v142, 8, v204
	ds_read_b128 v[142:145], v142
	ds_read_b128 v[146:149], v222
	s_waitcnt lgkmcnt(0)
	v_mfma_f32_16x16x32_bf16 v[134:137], v[142:145], v[146:149], v[134:137]
	v_or_b32_e32 v142, 2, v150
	v_mfma_f32_16x16x32_bf16 v[130:133], v[138:141], v[146:149], v[130:133]
	v_lshl_or_b32 v138, v142, 10, v198
	ds_read_b128 v[138:141], v138
	v_lshl_or_b32 v142, v142, 8, v204
	ds_read_b128 v[142:145], v142
	ds_read_b128 v[146:149], v221
	s_waitcnt lgkmcnt(0)
	v_mfma_f32_16x16x32_bf16 v[134:137], v[142:145], v[146:149], v[134:137]
	v_or_b32_e32 v142, 3, v150
	v_mfma_f32_16x16x32_bf16 v[130:133], v[138:141], v[146:149], v[130:133]
	v_lshl_or_b32 v138, v142, 10, v198
	ds_read_b128 v[138:141], v138
	v_lshl_or_b32 v142, v142, 8, v204
	ds_read_b128 v[142:145], v142
	ds_read_b128 v[146:149], v219
	s_waitcnt lgkmcnt(0)
	v_mfma_f32_16x16x32_bf16 v[134:137], v[142:145], v[146:149], v[134:137]
	v_or_b32_e32 v142, 4, v150
	v_mfma_f32_16x16x32_bf16 v[130:133], v[138:141], v[146:149], v[130:133]
	v_lshl_or_b32 v138, v142, 10, v198
	ds_read_b128 v[138:141], v138
	v_lshl_or_b32 v142, v142, 8, v204
	ds_read_b128 v[142:145], v142
	ds_read_b128 v[146:149], v218
	s_waitcnt lgkmcnt(0)
	v_mfma_f32_16x16x32_bf16 v[134:137], v[142:145], v[146:149], v[134:137]
	v_or_b32_e32 v142, 5, v150
	v_mfma_f32_16x16x32_bf16 v[130:133], v[138:141], v[146:149], v[130:133]
	v_lshl_or_b32 v138, v142, 10, v198
	ds_read_b128 v[138:141], v138
	v_lshl_or_b32 v142, v142, 8, v204
	ds_read_b128 v[142:145], v142
	ds_read_b128 v[146:149], v217
	s_waitcnt lgkmcnt(0)
	v_mfma_f32_16x16x32_bf16 v[134:137], v[142:145], v[146:149], v[134:137]
	v_or_b32_e32 v142, 6, v150
	v_mfma_f32_16x16x32_bf16 v[130:133], v[138:141], v[146:149], v[130:133]
	v_lshl_or_b32 v138, v142, 10, v198
	ds_read_b128 v[138:141], v138
	v_lshl_or_b32 v142, v142, 8, v204
	ds_read_b128 v[142:145], v142
	ds_read_b128 v[146:149], v216
	s_waitcnt lgkmcnt(0)
	v_mfma_f32_16x16x32_bf16 v[134:137], v[142:145], v[146:149], v[134:137]
	v_or_b32_e32 v142, 7, v150
	v_mfma_f32_16x16x32_bf16 v[130:133], v[138:141], v[146:149], v[130:133]
	v_lshl_or_b32 v138, v142, 10, v198
	v_lshl_or_b32 v142, v142, 8, v204
	ds_read_b128 v[138:141], v138
	ds_read_b128 v[142:145], v142
	ds_read_b128 v[146:149], v213
	ds_write_b64 v212, v[6:7]
	s_waitcnt vmcnt(18)
	v_cvt_pk_bf16_f32 v6, v18, v19
	v_cvt_pk_bf16_f32 v7, v20, v21
	ds_write_b64 v211, v[6:7] offset:512
	s_waitcnt vmcnt(17)
	v_cvt_pk_bf16_f32 v6, v26, v27
	v_cvt_pk_bf16_f32 v7, v28, v29
	ds_write_b64 v210, v[6:7] offset:1024
	s_waitcnt vmcnt(16)
	v_cvt_pk_bf16_f32 v6, v34, v35
	v_cvt_pk_bf16_f32 v7, v36, v37
	ds_write_b64 v209, v[6:7] offset:1536
	v_cvt_pk_bf16_f32 v6, v42, v43
	v_cvt_pk_bf16_f32 v7, v44, v45
	ds_write_b64 v208, v[6:7] offset:2048
	v_cvt_pk_bf16_f32 v6, v50, v51
	v_cvt_pk_bf16_f32 v7, v52, v53
	ds_write_b64 v207, v[6:7] offset:2560
	v_cvt_pk_bf16_f32 v6, v58, v59
	v_cvt_pk_bf16_f32 v7, v60, v61
	ds_write_b64 v206, v[6:7] offset:3072
	v_cvt_pk_bf16_f32 v6, v66, v67
	v_cvt_pk_bf16_f32 v7, v68, v69
	ds_write_b64 v205, v[6:7] offset:3584
	v_cvt_pk_bf16_f32 v6, v74, v75
	v_cvt_pk_bf16_f32 v7, v76, v77
	ds_write_b64 v231, v[6:7] offset:4096
	v_cvt_pk_bf16_f32 v6, v82, v83
	v_cvt_pk_bf16_f32 v7, v84, v85
	ds_write_b64 v230, v[6:7] offset:4608
	v_cvt_pk_bf16_f32 v6, v90, v91
	v_cvt_pk_bf16_f32 v7, v92, v93
	ds_write_b64 v229, v[6:7] offset:5120
	v_cvt_pk_bf16_f32 v6, v98, v99
	v_cvt_pk_bf16_f32 v7, v100, v101
	ds_write_b64 v228, v[6:7] offset:5632
	v_cvt_pk_bf16_f32 v6, v102, v103
	v_cvt_pk_bf16_f32 v7, v104, v105
	ds_write_b64 v227, v[6:7] offset:6144
	v_cvt_pk_bf16_f32 v6, v110, v111
	v_cvt_pk_bf16_f32 v7, v112, v113
	ds_write_b64 v226, v[6:7] offset:6656
	v_cvt_pk_bf16_f32 v6, v118, v119
	v_cvt_pk_bf16_f32 v7, v120, v121
	ds_write_b64 v225, v[6:7] offset:7168
	v_cvt_pk_bf16_f32 v6, v126, v127
	v_cvt_pk_bf16_f32 v7, v128, v129
	ds_write_b64 v224, v[6:7] offset:7680
	v_add_u32_e32 v6, 0x1800, v196
	v_and_or_b32 v126, v6, s0, v203
	buffer_load_dwordx4 v[6:9], v126, s[4:7], 0 offen nt
	v_or_b32_e32 v18, 0x2000, v126
	v_or_b32_e32 v26, 0x4000, v126
	v_or_b32_e32 v34, 0x6000, v126
	v_or_b32_e32 v42, 0x8000, v126
	v_or_b32_e32 v50, 0xa000, v126
	v_or_b32_e32 v58, 0xc000, v126
	v_or_b32_e32 v66, 0xe000, v126
	v_or_b32_e32 v74, 0x10000, v126
	v_or_b32_e32 v82, 0x12000, v126
	v_or_b32_e32 v90, 0x14000, v126
	v_or_b32_e32 v98, 0x16000, v126
	v_or_b32_e32 v102, 0x18000, v126
	v_or_b32_e32 v110, 0x1a000, v126
	v_or_b32_e32 v118, 0x1c000, v126
	v_or_b32_e32 v126, 0x1e000, v126
	buffer_load_dwordx4 v[50:53], v50, s[4:7], 0 offen nt
	s_waitcnt lgkmcnt(14)
	v_mfma_f32_16x16x32_bf16 v[130:133], v[138:141], v[146:149], v[130:133]
	buffer_load_dwordx4 v[58:61], v58, s[4:7], 0 offen nt
	s_nop 0
	buffer_load_dwordx4 v[66:69], v66, s[4:7], 0 offen nt
	v_mfma_f32_16x16x32_bf16 v[134:137], v[142:145], v[146:149], v[134:137]
	buffer_load_dwordx4 v[74:77], v74, s[4:7], 0 offen nt
	v_add_u32_e32 v142, 7, v200
	buffer_load_dwordx4 v[82:85], v82, s[4:7], 0 offen nt
	s_nop 0
	buffer_load_dwordx4 v[90:93], v90, s[4:7], 0 offen nt
	s_nop 0
	buffer_load_dwordx4 v[98:101], v98, s[4:7], 0 offen nt
	s_nop 0
	buffer_load_dwordx4 v[102:105], v102, s[4:7], 0 offen nt
	s_nop 0
	buffer_load_dwordx4 v[110:113], v110, s[4:7], 0 offen nt
	s_nop 0
	buffer_load_dwordx4 v[118:121], v118, s[4:7], 0 offen nt
	s_nop 0
	buffer_load_dwordx4 v[126:129], v126, s[4:7], 0 offen nt
	s_nop 0
	buffer_load_dwordx4 v[18:21], v18, s[4:7], 0 offen nt
	s_nop 0
	buffer_load_dwordx4 v[26:29], v26, s[4:7], 0 offen nt
	s_nop 0
	buffer_load_dwordx4 v[34:37], v34, s[4:7], 0 offen nt
	s_nop 0
	buffer_load_dwordx4 v[42:45], v42, s[4:7], 0 offen nt
	v_xor_b32_e32 v143, 32, v232
	v_lshl_or_b32 v138, v143, 10, v198
	ds_read_b128 v[138:141], v138
	v_lshl_or_b32 v143, v143, 8, v204
	ds_read_b128 v[144:147], v143
	ds_read_b128 v[148:151], v223
	v_bitop3_b32 v143, v232, 1, 32 bitop3:0xde
	s_waitcnt vmcnt(31)
	v_cvt_pk_bf16_f32 v2, v2, v3
	s_waitcnt lgkmcnt(0)
	v_mfma_f32_16x16x32_bf16 v[134:137], v[144:147], v[148:151], v[134:137]
	v_cvt_pk_bf16_f32 v3, v4, v5
	v_mfma_f32_16x16x32_bf16 v[130:133], v[138:141], v[148:151], v[130:133]
	v_lshl_or_b32 v138, v143, 10, v198
	ds_read_b128 v[138:141], v138
	v_lshl_or_b32 v143, v143, 8, v204
	ds_read_b128 v[144:147], v143
	ds_read_b128 v[148:151], v222
	v_bitop3_b32 v143, v232, 2, 32 bitop3:0xde
	s_waitcnt lgkmcnt(0)
	v_mfma_f32_16x16x32_bf16 v[134:137], v[144:147], v[148:151], v[134:137]
	v_mfma_f32_16x16x32_bf16 v[130:133], v[138:141], v[148:151], v[130:133]
	v_lshl_or_b32 v138, v143, 10, v198
	ds_read_b128 v[138:141], v138
	v_lshl_or_b32 v143, v143, 8, v204
	ds_read_b128 v[144:147], v143
	ds_read_b128 v[148:151], v221
	v_bitop3_b32 v143, v232, 3, 32 bitop3:0xde
	s_waitcnt lgkmcnt(0)
	v_mfma_f32_16x16x32_bf16 v[130:133], v[138:141], v[148:151], v[130:133]
	v_lshl_or_b32 v138, v143, 10, v198
	ds_read_b128 v[138:141], v138
	v_lshl_or_b32 v143, v143, 8, v204
	v_mfma_f32_16x16x32_bf16 v[134:137], v[144:147], v[148:151], v[134:137]
	ds_read_b128 v[144:147], v143
	ds_read_b128 v[148:151], v219
	v_bitop3_b32 v143, v232, 4, 32 bitop3:0xde
	s_waitcnt lgkmcnt(0)
	v_mfma_f32_16x16x32_bf16 v[130:133], v[138:141], v[148:151], v[130:133]
	v_lshl_or_b32 v138, v143, 10, v198
	ds_read_b128 v[138:141], v138
	v_lshl_or_b32 v143, v143, 8, v204
	v_mfma_f32_16x16x32_bf16 v[134:137], v[144:147], v[148:151], v[134:137]
	ds_read_b128 v[144:147], v143
	ds_read_b128 v[148:151], v218
	v_bitop3_b32 v143, v232, 5, 32 bitop3:0xde
	s_waitcnt lgkmcnt(0)
	v_mfma_f32_16x16x32_bf16 v[130:133], v[138:141], v[148:151], v[130:133]
	v_lshl_or_b32 v138, v143, 10, v198
	ds_read_b128 v[138:141], v138
	v_lshl_or_b32 v143, v143, 8, v204
	v_mfma_f32_16x16x32_bf16 v[134:137], v[144:147], v[148:151], v[134:137]
	ds_read_b128 v[144:147], v143
	ds_read_b128 v[148:151], v217
	v_bitop3_b32 v143, v232, 6, 32 bitop3:0xde
	s_waitcnt lgkmcnt(0)
	v_mfma_f32_16x16x32_bf16 v[130:133], v[138:141], v[148:151], v[130:133]
	v_lshl_or_b32 v138, v143, 10, v198
	ds_read_b128 v[138:141], v138
	v_lshl_or_b32 v143, v143, 8, v204
	v_mfma_f32_16x16x32_bf16 v[134:137], v[144:147], v[148:151], v[134:137]
	ds_read_b128 v[144:147], v143
	ds_read_b128 v[148:151], v216
	v_bitop3_b32 v143, v232, 7, 32 bitop3:0xde
	s_waitcnt lgkmcnt(0)
	v_mfma_f32_16x16x32_bf16 v[130:133], v[138:141], v[148:151], v[130:133]
	v_lshl_or_b32 v138, v143, 10, v198
	v_lshl_or_b32 v143, v143, 8, v204
	ds_read_b128 v[138:141], v138
	v_mfma_f32_16x16x32_bf16 v[134:137], v[144:147], v[148:151], v[134:137]
	ds_read_b128 v[144:147], v143
	ds_read_b128 v[148:151], v213
	ds_write_b64 v212, v[2:3]
	s_waitcnt vmcnt(21)
	v_cvt_pk_bf16_f32 v2, v10, v11
	v_cvt_pk_bf16_f32 v3, v12, v13
	ds_write_b64 v211, v[2:3] offset:512
	s_waitcnt vmcnt(20)
	v_cvt_pk_bf16_f32 v2, v14, v15
	v_cvt_pk_bf16_f32 v3, v16, v17
	ds_write_b64 v210, v[2:3] offset:1024
	s_waitcnt vmcnt(19)
	v_cvt_pk_bf16_f32 v2, v22, v23
	v_cvt_pk_bf16_f32 v3, v24, v25
	ds_write_b64 v209, v[2:3] offset:1536
	s_waitcnt vmcnt(18)
	v_cvt_pk_bf16_f32 v2, v30, v31
	v_cvt_pk_bf16_f32 v3, v32, v33
	ds_write_b64 v208, v[2:3] offset:2048
	s_waitcnt vmcnt(17)
	v_cvt_pk_bf16_f32 v2, v38, v39
	v_cvt_pk_bf16_f32 v3, v40, v41
	ds_write_b64 v207, v[2:3] offset:2560
	s_waitcnt vmcnt(16)
	v_cvt_pk_bf16_f32 v2, v46, v47
	v_cvt_pk_bf16_f32 v3, v48, v49
	ds_write_b64 v206, v[2:3] offset:3072
	v_cvt_pk_bf16_f32 v2, v54, v55
	v_cvt_pk_bf16_f32 v3, v56, v57
	ds_write_b64 v205, v[2:3] offset:3584
	v_cvt_pk_bf16_f32 v2, v62, v63
	v_cvt_pk_bf16_f32 v3, v64, v65
	ds_write_b64 v231, v[2:3] offset:4096
	v_cvt_pk_bf16_f32 v2, v70, v71
	v_cvt_pk_bf16_f32 v3, v72, v73
	ds_write_b64 v230, v[2:3] offset:4608
	v_cvt_pk_bf16_f32 v2, v78, v79
	v_cvt_pk_bf16_f32 v3, v80, v81
	ds_write_b64 v229, v[2:3] offset:5120
	v_cvt_pk_bf16_f32 v2, v86, v87
	v_cvt_pk_bf16_f32 v3, v88, v89
	ds_write_b64 v228, v[2:3] offset:5632
	v_cvt_pk_bf16_f32 v2, v94, v95
	v_cvt_pk_bf16_f32 v3, v96, v97
	ds_write_b64 v227, v[2:3] offset:6144
	v_cvt_pk_bf16_f32 v2, v106, v107
	v_cvt_pk_bf16_f32 v3, v108, v109
	ds_write_b64 v226, v[2:3] offset:6656
	v_cvt_pk_bf16_f32 v2, v114, v115
	v_cvt_pk_bf16_f32 v3, v116, v117
	ds_write_b64 v225, v[2:3] offset:7168
	v_cvt_pk_bf16_f32 v2, v122, v123
	v_cvt_pk_bf16_f32 v3, v124, v125
	ds_write_b64 v224, v[2:3] offset:7680
	v_lshlrev_b32_e32 v2, 10, v142
	v_and_or_b32 v2, v2, s0, v203
	v_or_b32_e32 v3, 0x2000, v2
	buffer_load_dwordx4 v[10:13], v2, s[4:7], 0 offen nt
	buffer_load_dwordx4 v[14:17], v3, s[4:7], 0 offen nt
	v_or_b32_e32 v3, 0x4000, v2
	buffer_load_dwordx4 v[22:25], v3, s[4:7], 0 offen nt
	v_or_b32_e32 v3, 0x6000, v2
	buffer_load_dwordx4 v[30:33], v3, s[4:7], 0 offen nt
	v_or_b32_e32 v3, 0x8000, v2
	buffer_load_dwordx4 v[38:41], v3, s[4:7], 0 offen nt
	v_or_b32_e32 v3, 0xa000, v2
	buffer_load_dwordx4 v[46:49], v3, s[4:7], 0 offen nt
	v_or_b32_e32 v3, 0xc000, v2
	buffer_load_dwordx4 v[54:57], v3, s[4:7], 0 offen nt
	v_or_b32_e32 v3, 0xe000, v2
	buffer_load_dwordx4 v[62:65], v3, s[4:7], 0 offen nt
	v_or_b32_e32 v3, 0x10000, v2
	buffer_load_dwordx4 v[70:73], v3, s[4:7], 0 offen nt
	v_or_b32_e32 v3, 0x12000, v2
	buffer_load_dwordx4 v[78:81], v3, s[4:7], 0 offen nt
	v_or_b32_e32 v3, 0x14000, v2
	buffer_load_dwordx4 v[86:89], v3, s[4:7], 0 offen nt
	v_or_b32_e32 v3, 0x16000, v2
	buffer_load_dwordx4 v[94:97], v3, s[4:7], 0 offen nt
	v_or_b32_e32 v3, 0x18000, v2
	buffer_load_dwordx4 v[106:109], v3, s[4:7], 0 offen nt
	v_or_b32_e32 v3, 0x1a000, v2
	buffer_load_dwordx4 v[114:117], v3, s[4:7], 0 offen nt
	v_or_b32_e32 v3, 0x1c000, v2
	v_or_b32_e32 v2, 0x1e000, v2
	s_waitcnt lgkmcnt(14)
	v_mfma_f32_16x16x32_bf16 v[138:141], v[138:141], v[148:151], v[130:133]
	buffer_load_dwordx4 v[122:125], v3, s[4:7], 0 offen nt
	s_nop 1
	buffer_load_dwordx4 v[130:133], v2, s[4:7], 0 offen nt
	v_mfma_f32_16x16x32_bf16 v[134:137], v[144:147], v[148:151], v[134:137]
	v_lshlrev_b32_e32 v2, 3, v234
	v_and_b32_e32 v143, 56, v2
	v_lshl_or_b32 v2, v143, 10, v198
	v_lshl_or_b32 v152, v143, 8, v204
	ds_read_b128 v[2:5], v2
	ds_read_b128 v[144:147], v223
	ds_read_b128 v[148:151], v222
	ds_read_b128 v[152:155], v152
	v_or_b32_e32 v156, 1, v143
	v_lshl_or_b32 v157, v156, 10, v198
	s_waitcnt lgkmcnt(2)
	v_mfma_f32_16x16x32_bf16 v[2:5], v[2:5], v[144:147], v[138:141]
	s_waitcnt vmcnt(31)
	v_cvt_pk_bf16_f32 v6, v6, v7
	v_cvt_pk_bf16_f32 v7, v8, v9
	s_waitcnt lgkmcnt(0)
	v_mfma_f32_16x16x32_bf16 v[134:137], v[152:155], v[144:147], v[134:137]
	ds_read_b128 v[138:141], v157
	v_lshl_or_b32 v144, v156, 8, v204
	ds_read_b128 v[144:147], v144
	v_or_b32_e32 v156, 2, v143
	s_waitcnt lgkmcnt(1)
	v_mfma_f32_16x16x32_bf16 v[2:5], v[138:141], v[148:151], v[2:5]
	v_lshl_or_b32 v138, v156, 10, v198
	ds_read_b128 v[138:141], v138
	ds_read_b128 v[152:155], v221
	s_waitcnt lgkmcnt(2)
	v_mfma_f32_16x16x32_bf16 v[134:137], v[144:147], v[148:151], v[134:137]
	v_lshl_or_b32 v144, v156, 8, v204
	v_or_b32_e32 v156, 3, v143
	ds_read_b128 v[144:147], v144
	ds_read_b128 v[148:151], v219
	s_waitcnt lgkmcnt(2)
	v_mfma_f32_16x16x32_bf16 v[2:5], v[138:141], v[152:155], v[2:5]
	v_lshl_or_b32 v138, v156, 10, v198
	ds_read_b128 v[138:141], v138
	s_waitcnt lgkmcnt(2)
	v_mfma_f32_16x16x32_bf16 v[134:137], v[144:147], v[152:155], v[134:137]
	v_lshl_or_b32 v144, v156, 8, v204
	ds_read_b128 v[144:147], v144
	v_or_b32_e32 v152, 4, v143
	s_waitcnt lgkmcnt(1)
	v_mfma_f32_16x16x32_bf16 v[2:5], v[138:141], v[148:151], v[2:5]
	v_lshl_or_b32 v138, v152, 10, v198
	ds_read_b128 v[138:141], v138
	v_or_b32_e32 v156, 5, v143
	s_waitcnt lgkmcnt(1)
	v_mfma_f32_16x16x32_bf16 v[134:137], v[144:147], v[148:151], v[134:137]
	ds_read_b128 v[144:147], v218
	v_lshl_or_b32 v148, v152, 8, v204
	ds_read_b128 v[148:151], v148
	ds_read_b128 v[152:155], v217
	s_waitcnt lgkmcnt(2)
	v_mfma_f32_16x16x32_bf16 v[2:5], v[138:141], v[144:147], v[2:5]
	v_lshl_or_b32 v138, v156, 10, v198
	ds_read_b128 v[138:141], v138
	s_waitcnt lgkmcnt(2)
	v_mfma_f32_16x16x32_bf16 v[134:137], v[148:151], v[144:147], v[134:137]
	v_lshl_or_b32 v144, v156, 8, v204
	ds_read_b128 v[144:147], v144
	v_or_b32_e32 v148, 6, v143
	s_waitcnt lgkmcnt(1)
	v_mfma_f32_16x16x32_bf16 v[2:5], v[138:141], v[152:155], v[2:5]
	v_lshl_or_b32 v138, v148, 10, v198
	ds_read_b128 v[138:141], v138
	v_lshl_or_b32 v148, v148, 8, v204
	s_waitcnt lgkmcnt(1)
	v_mfma_f32_16x16x32_bf16 v[134:137], v[144:147], v[152:155], v[134:137]
	ds_read_b128 v[144:147], v216
	ds_read_b128 v[148:151], v148
	ds_read_b128 v[152:155], v213
	v_or_b32_e32 v143, 7, v143
	ds_write_b64 v212, v[6:7]
	s_waitcnt lgkmcnt(3)
	v_mfma_f32_16x16x32_bf16 v[2:5], v[138:141], v[144:147], v[2:5]
	v_lshl_or_b32 v138, v143, 10, v198
	v_lshl_or_b32 v143, v143, 8, v204
	s_waitcnt vmcnt(19)
	v_cvt_pk_bf16_f32 v6, v18, v19
	v_cvt_pk_bf16_f32 v7, v20, v21
	ds_read_b128 v[138:141], v138
	s_waitcnt lgkmcnt(3)
	v_mfma_f32_16x16x32_bf16 v[134:137], v[148:151], v[144:147], v[134:137]
	ds_read_b128 v[144:147], v143
	ds_write_b64 v211, v[6:7] offset:512
	s_waitcnt vmcnt(18)
	v_cvt_pk_bf16_f32 v6, v26, v27
	v_cvt_pk_bf16_f32 v7, v28, v29
	ds_write_b64 v210, v[6:7] offset:1024
	s_waitcnt vmcnt(17)
	v_cvt_pk_bf16_f32 v6, v34, v35
	v_cvt_pk_bf16_f32 v7, v36, v37
	ds_write_b64 v209, v[6:7] offset:1536
	s_waitcnt vmcnt(16)
	v_cvt_pk_bf16_f32 v6, v42, v43
	v_cvt_pk_bf16_f32 v7, v44, v45
	ds_write_b64 v208, v[6:7] offset:2048
	v_cvt_pk_bf16_f32 v6, v50, v51
	v_cvt_pk_bf16_f32 v7, v52, v53
	ds_write_b64 v207, v[6:7] offset:2560
	v_cvt_pk_bf16_f32 v6, v58, v59
	v_cvt_pk_bf16_f32 v7, v60, v61
	ds_write_b64 v206, v[6:7] offset:3072
	v_cvt_pk_bf16_f32 v6, v66, v67
	v_cvt_pk_bf16_f32 v7, v68, v69
	ds_write_b64 v205, v[6:7] offset:3584
	v_cvt_pk_bf16_f32 v6, v74, v75
	v_cvt_pk_bf16_f32 v7, v76, v77
	ds_write_b64 v231, v[6:7] offset:4096
	v_cvt_pk_bf16_f32 v6, v82, v83
	v_cvt_pk_bf16_f32 v7, v84, v85
	ds_write_b64 v230, v[6:7] offset:4608
	v_cvt_pk_bf16_f32 v6, v90, v91
	v_cvt_pk_bf16_f32 v7, v92, v93
	s_waitcnt lgkmcnt(9)
	v_mfma_f32_16x16x32_bf16 v[134:137], v[144:147], v[152:155], v[134:137]
	ds_write_b64 v229, v[6:7] offset:5120
	v_cvt_pk_bf16_f32 v6, v98, v99
	v_cvt_pk_bf16_f32 v7, v100, v101
	ds_write_b64 v228, v[6:7] offset:5632
	v_cvt_pk_bf16_f32 v6, v102, v103
	v_cvt_pk_bf16_f32 v7, v104, v105
	ds_write_b64 v227, v[6:7] offset:6144
	v_cvt_pk_bf16_f32 v6, v110, v111
	v_cvt_pk_bf16_f32 v7, v112, v113
	ds_write_b64 v226, v[6:7] offset:6656
	v_cvt_pk_bf16_f32 v6, v118, v119
	v_cvt_pk_bf16_f32 v7, v120, v121
	v_mfma_f32_16x16x32_bf16 v[2:5], v[138:141], v[152:155], v[2:5]
	ds_write_b64 v225, v[6:7] offset:7168
	v_cvt_pk_bf16_f32 v6, v126, v127
	v_cvt_pk_bf16_f32 v7, v128, v129
	ds_write_b64 v224, v[6:7] offset:7680
	v_add_u32_e32 v6, 48, v232
	v_and_b32_e32 v50, 56, v6
	v_lshl_or_b32 v6, v50, 10, v198
	v_lshl_or_b32 v34, v50, 8, v204
	ds_read_b128 v[6:9], v6
	ds_read_b128 v[18:21], v223
	ds_read_b128 v[26:29], v222
	ds_read_b128 v[34:37], v34
	v_or_b32_e32 v42, 1, v50
	v_lshl_or_b32 v43, v42, 10, v198
	s_waitcnt lgkmcnt(2)
	v_mfma_f32_16x16x32_bf16 v[2:5], v[6:9], v[18:21], v[2:5]
	ds_read_b128 v[6:9], v43
	v_or_b32_e32 v51, 2, v50
	s_waitcnt lgkmcnt(1)
	v_mfma_f32_16x16x32_bf16 v[18:21], v[34:37], v[18:21], v[134:137]
	v_lshl_or_b32 v34, v42, 8, v204
	ds_read_b128 v[34:37], v34
	s_waitcnt lgkmcnt(1)
	v_mfma_f32_16x16x32_bf16 v[2:5], v[6:9], v[26:29], v[2:5]
	v_lshl_or_b32 v6, v51, 10, v198
	ds_read_b128 v[6:9], v6
	ds_read_b128 v[42:45], v221
	s_waitcnt lgkmcnt(2)
	v_mfma_f32_16x16x32_bf16 v[18:21], v[34:37], v[26:29], v[18:21]
	v_lshl_or_b32 v26, v51, 8, v204
	v_or_b32_e32 v51, 3, v50
	ds_read_b128 v[26:29], v26
	ds_read_b128 v[34:37], v219
	s_waitcnt lgkmcnt(2)
	v_mfma_f32_16x16x32_bf16 v[2:5], v[6:9], v[42:45], v[2:5]
	v_lshl_or_b32 v6, v51, 10, v198
	ds_read_b128 v[6:9], v6
	s_waitcnt lgkmcnt(2)
	v_mfma_f32_16x16x32_bf16 v[18:21], v[26:29], v[42:45], v[18:21]
	v_lshl_or_b32 v26, v51, 8, v204
	ds_read_b128 v[26:29], v26
	v_or_b32_e32 v42, 4, v50
	s_waitcnt lgkmcnt(1)
	v_mfma_f32_16x16x32_bf16 v[2:5], v[6:9], v[34:37], v[2:5]
	v_lshl_or_b32 v6, v42, 10, v198
	ds_read_b128 v[6:9], v6
	v_or_b32_e32 v51, 5, v50
	s_waitcnt lgkmcnt(1)
	v_mfma_f32_16x16x32_bf16 v[18:21], v[26:29], v[34:37], v[18:21]
	ds_read_b128 v[26:29], v218
	v_lshl_or_b32 v34, v42, 8, v204
	ds_read_b128 v[34:37], v34
	ds_read_b128 v[42:45], v217
	s_waitcnt lgkmcnt(2)
	v_mfma_f32_16x16x32_bf16 v[2:5], v[6:9], v[26:29], v[2:5]
	v_lshl_or_b32 v6, v51, 10, v198
	ds_read_b128 v[6:9], v6
	s_waitcnt lgkmcnt(2)
	v_mfma_f32_16x16x32_bf16 v[18:21], v[34:37], v[26:29], v[18:21]
	v_lshl_or_b32 v26, v51, 8, v204
	ds_read_b128 v[26:29], v26
	v_or_b32_e32 v34, 6, v50
	s_waitcnt lgkmcnt(1)
	v_mfma_f32_16x16x32_bf16 v[2:5], v[6:9], v[42:45], v[2:5]
	v_lshl_or_b32 v6, v34, 10, v198
	ds_read_b128 v[6:9], v6
	v_lshl_or_b32 v34, v34, 8, v204
	s_waitcnt lgkmcnt(1)
	v_mfma_f32_16x16x32_bf16 v[18:21], v[26:29], v[42:45], v[18:21]
	ds_read_b128 v[26:29], v216
	ds_read_b128 v[34:37], v34
	ds_read_b128 v[42:45], v213
	v_or_b32_e32 v50, 7, v50
	s_waitcnt lgkmcnt(2)
	v_mfma_f32_16x16x32_bf16 v[2:5], v[6:9], v[26:29], v[2:5]
	v_lshl_or_b32 v6, v50, 10, v198
	ds_read_b128 v[6:9], v6
	s_waitcnt lgkmcnt(2)
	v_mfma_f32_16x16x32_bf16 v[18:21], v[34:37], v[26:29], v[18:21]
	v_lshl_or_b32 v26, v50, 8, v204
	ds_read_b128 v[26:29], v26
	s_waitcnt lgkmcnt(1)
	v_mfma_f32_16x16x32_bf16 v[34:37], v[6:9], v[42:45], v[2:5]
	v_and_b32_e32 v74, 7, v197
	v_lshrrev_b32_e32 v75, 3, v197
	v_lshlrev_b32_e32 v192, 13, v200
	v_lshlrev_b32_e32 v193, 11, v200
	v_lshl_add_u32 v203, v197, 2, v196
	v_lshl_or_b32 v192, v75, 8, v192
	v_lshl_or_b32 v193, v75, 6, v193
	v_add_u32_e32 v203, 0x24800, v203
	v_lshl_or_b32 v192, v201, 6, v192
	v_lshl_or_b32 v193, v74, 1, v193
	v_lshl_or_b32 v192, v74, 1, v192
	v_or_b32_e32 v193, 0x10000, v193
	v_cmp_gt_u32_e64 s[36:37], 16, v1
	v_cmp_eq_u32_e64 s[38:39], 1, v201
	ds_read2_b32 v[2:3], v203 offset1:16
	ds_read2_b32 v[4:5], v203 offset0:32 offset1:48
	ds_read2_b32 v[6:7], v203 offset0:64 offset1:80
	ds_read2_b32 v[8:9], v203 offset0:96 offset1:112
	ds_read2_b32 v[50:51], v203 offset0:128 offset1:144
	ds_read2_b32 v[52:53], v203 offset0:160 offset1:176
	ds_read2_b32 v[58:59], v203 offset0:192 offset1:208
	ds_read2_b32 v[60:61], v203 offset0:224 offset1:240
	v_mov_b32_e32 v146, 0
	v_mov_b32_e32 v147, 0
	v_mov_b32_e32 v150, 0
	v_mov_b32_e32 v151, 0
	v_mov_b32_e32 v154, 0
	v_mov_b32_e32 v155, 0
	v_mov_b32_e32 v158, 0
	v_mov_b32_e32 v159, 0
	v_mov_b32_e32 v162, 0
	v_mov_b32_e32 v163, 0
	v_mov_b32_e32 v166, 0
	v_mov_b32_e32 v167, 0
	v_mov_b32_e32 v170, 0
	v_mov_b32_e32 v171, 0
	v_mov_b32_e32 v174, 0
	v_mov_b32_e32 v175, 0
	v_mov_b32_e32 v178, 0
	v_mov_b32_e32 v179, 0
	v_mov_b32_e32 v182, 0
	v_mov_b32_e32 v183, 0
	v_mov_b32_e32 v186, 0
	v_mov_b32_e32 v187, 0
	v_mov_b32_e32 v190, 0
	v_mov_b32_e32 v191, 0
	v_mov_b32_e32 v234, 0
	v_mov_b32_e32 v235, 0
	v_mov_b32_e32 v238, 0
	v_mov_b32_e32 v239, 0
	v_mov_b32_e32 v242, 0
	v_mov_b32_e32 v243, 0
	v_mov_b32_e32 v246, 0
	v_mov_b32_e32 v247, 0
	ds_read_u16 v82, v192
	ds_read_u16 v83, v192 offset:16
	ds_read_u16 v84, v192 offset:32
	ds_read_u16 v85, v192 offset:48
	ds_read_u16 v90, v193
	ds_read_u16 v91, v193 offset:16
	ds_read_u16 v92, v193 offset:32
	ds_read_u16 v93, v193 offset:48
	ds_read_u16 v98, v192 offset:512
	ds_read_u16 v99, v192 offset:528
	ds_read_u16 v100, v192 offset:544
	ds_read_u16 v101, v192 offset:560
	ds_read_u16 v102, v193 offset:128
	ds_read_u16 v103, v193 offset:144
	ds_read_u16 v104, v193 offset:160
	ds_read_u16 v105, v193 offset:176
	s_waitcnt lgkmcnt(8)
	v_lshl_or_b32 v144, v83, 16, v82
	v_lshl_or_b32 v145, v85, 16, v84
	s_mov_b64 exec, s[36:37]
	v_lshl_or_b32 v146, v91, 16, v90
	v_lshl_or_b32 v147, v93, 16, v92
	s_mov_b64 exec, -1
	ds_read_u16 v82, v192 offset:1024
	ds_read_u16 v83, v192 offset:1040
	ds_read_u16 v84, v192 offset:1056
	ds_read_u16 v85, v192 offset:1072
	ds_read_u16 v90, v193 offset:256
	ds_read_u16 v91, v193 offset:272
	ds_read_u16 v92, v193 offset:288
	ds_read_u16 v93, v193 offset:304
	s_waitcnt lgkmcnt(8)
	v_lshl_or_b32 v148, v99, 16, v98
	v_lshl_or_b32 v149, v101, 16, v100
	s_mov_b64 exec, s[36:37]
	v_lshl_or_b32 v150, v103, 16, v102
	v_lshl_or_b32 v151, v105, 16, v104
	s_mov_b64 exec, -1
	ds_read_u16 v98, v192 offset:1536
	ds_read_u16 v99, v192 offset:1552
	ds_read_u16 v100, v192 offset:1568
	ds_read_u16 v101, v192 offset:1584
	ds_read_u16 v102, v193 offset:384
	ds_read_u16 v103, v193 offset:400
	ds_read_u16 v104, v193 offset:416
	ds_read_u16 v105, v193 offset:432
	s_waitcnt lgkmcnt(8)
	v_lshl_or_b32 v152, v83, 16, v82
	v_lshl_or_b32 v153, v85, 16, v84
	s_mov_b64 exec, s[36:37]
	v_lshl_or_b32 v154, v91, 16, v90
	v_lshl_or_b32 v155, v93, 16, v92
	s_mov_b64 exec, -1
	ds_read_u16 v82, v192 offset:2048
	ds_read_u16 v83, v192 offset:2064
	ds_read_u16 v84, v192 offset:2080
	ds_read_u16 v85, v192 offset:2096
	ds_read_u16 v90, v193 offset:512
	ds_read_u16 v91, v193 offset:528
	ds_read_u16 v92, v193 offset:544
	ds_read_u16 v93, v193 offset:560
	s_waitcnt lgkmcnt(8)
	v_lshl_or_b32 v156, v99, 16, v98
	v_lshl_or_b32 v157, v101, 16, v100
	s_mov_b64 exec, s[36:37]
	v_lshl_or_b32 v158, v103, 16, v102
	v_lshl_or_b32 v159, v105, 16, v104
	s_mov_b64 exec, -1
	ds_read_u16 v98, v192 offset:2560
	ds_read_u16 v99, v192 offset:2576
	ds_read_u16 v100, v192 offset:2592
	ds_read_u16 v101, v192 offset:2608
	ds_read_u16 v102, v193 offset:640
	ds_read_u16 v103, v193 offset:656
	ds_read_u16 v104, v193 offset:672
	ds_read_u16 v105, v193 offset:688
	s_waitcnt lgkmcnt(8)
	v_lshl_or_b32 v160, v83, 16, v82
	v_lshl_or_b32 v161, v85, 16, v84
	s_mov_b64 exec, s[36:37]
	v_lshl_or_b32 v162, v91, 16, v90
	v_lshl_or_b32 v163, v93, 16, v92
	s_mov_b64 exec, -1
	ds_read_u16 v82, v192 offset:3072
	ds_read_u16 v83, v192 offset:3088
	ds_read_u16 v84, v192 offset:3104
	ds_read_u16 v85, v192 offset:3120
	ds_read_u16 v90, v193 offset:768
	ds_read_u16 v91, v193 offset:784
	ds_read_u16 v92, v193 offset:800
	ds_read_u16 v93, v193 offset:816
	s_waitcnt lgkmcnt(8)
	v_lshl_or_b32 v164, v99, 16, v98
	v_lshl_or_b32 v165, v101, 16, v100
	s_mov_b64 exec, s[36:37]
	v_lshl_or_b32 v166, v103, 16, v102
	v_lshl_or_b32 v167, v105, 16, v104
	s_mov_b64 exec, -1
	ds_read_u16 v98, v192 offset:3584
	ds_read_u16 v99, v192 offset:3600
	ds_read_u16 v100, v192 offset:3616
	ds_read_u16 v101, v192 offset:3632
	ds_read_u16 v102, v193 offset:896
	ds_read_u16 v103, v193 offset:912
	ds_read_u16 v104, v193 offset:928
	ds_read_u16 v105, v193 offset:944
	s_waitcnt lgkmcnt(8)
	v_lshl_or_b32 v168, v83, 16, v82
	v_lshl_or_b32 v169, v85, 16, v84
	s_mov_b64 exec, s[36:37]
	v_lshl_or_b32 v170, v91, 16, v90
	v_lshl_or_b32 v171, v93, 16, v92
	s_mov_b64 exec, -1
	ds_read_u16 v82, v192 offset:4096
	ds_read_u16 v83, v192 offset:4112
	ds_read_u16 v84, v192 offset:4128
	ds_read_u16 v85, v192 offset:4144
	ds_read_u16 v90, v193 offset:1024
	ds_read_u16 v91, v193 offset:1040
	ds_read_u16 v92, v193 offset:1056
	ds_read_u16 v93, v193 offset:1072
	s_waitcnt lgkmcnt(8)
	v_lshl_or_b32 v172, v99, 16, v98
	v_lshl_or_b32 v173, v101, 16, v100
	s_mov_b64 exec, s[36:37]
	v_lshl_or_b32 v174, v103, 16, v102
	v_lshl_or_b32 v175, v105, 16, v104
	s_mov_b64 exec, -1
	ds_read_u16 v98, v192 offset:4608
	ds_read_u16 v99, v192 offset:4624
	ds_read_u16 v100, v192 offset:4640
	ds_read_u16 v101, v192 offset:4656
	ds_read_u16 v102, v193 offset:1152
	ds_read_u16 v103, v193 offset:1168
	ds_read_u16 v104, v193 offset:1184
	ds_read_u16 v105, v193 offset:1200
	s_waitcnt lgkmcnt(8)
	v_lshl_or_b32 v176, v83, 16, v82
	v_lshl_or_b32 v177, v85, 16, v84
	s_mov_b64 exec, s[36:37]
	v_lshl_or_b32 v178, v91, 16, v90
	v_lshl_or_b32 v179, v93, 16, v92
	s_mov_b64 exec, -1
	ds_read_u16 v82, v192 offset:5120
	ds_read_u16 v83, v192 offset:5136
	ds_read_u16 v84, v192 offset:5152
	ds_read_u16 v85, v192 offset:5168
	ds_read_u16 v90, v193 offset:1280
	ds_read_u16 v91, v193 offset:1296
	ds_read_u16 v92, v193 offset:1312
	ds_read_u16 v93, v193 offset:1328
	s_waitcnt lgkmcnt(8)
	v_lshl_or_b32 v180, v99, 16, v98
	v_lshl_or_b32 v181, v101, 16, v100
	s_mov_b64 exec, s[36:37]
	v_lshl_or_b32 v182, v103, 16, v102
	v_lshl_or_b32 v183, v105, 16, v104
	s_mov_b64 exec, -1
	ds_read_u16 v98, v192 offset:5632
	ds_read_u16 v99, v192 offset:5648
	ds_read_u16 v100, v192 offset:5664
	ds_read_u16 v101, v192 offset:5680
	ds_read_u16 v102, v193 offset:1408
	ds_read_u16 v103, v193 offset:1424
	ds_read_u16 v104, v193 offset:1440
	ds_read_u16 v105, v193 offset:1456
	s_waitcnt lgkmcnt(8)
	v_lshl_or_b32 v184, v83, 16, v82
	v_lshl_or_b32 v185, v85, 16, v84
	s_mov_b64 exec, s[36:37]
	v_lshl_or_b32 v186, v91, 16, v90
	v_lshl_or_b32 v187, v93, 16, v92
	s_mov_b64 exec, -1
	ds_read_u16 v82, v192 offset:6144
	ds_read_u16 v83, v192 offset:6160
	ds_read_u16 v84, v192 offset:6176
	ds_read_u16 v85, v192 offset:6192
	ds_read_u16 v90, v193 offset:1536
	ds_read_u16 v91, v193 offset:1552
	ds_read_u16 v92, v193 offset:1568
	ds_read_u16 v93, v193 offset:1584
	s_waitcnt lgkmcnt(8)
	v_lshl_or_b32 v188, v99, 16, v98
	v_lshl_or_b32 v189, v101, 16, v100
	s_mov_b64 exec, s[36:37]
	v_lshl_or_b32 v190, v103, 16, v102
	v_lshl_or_b32 v191, v105, 16, v104
	s_mov_b64 exec, -1
	ds_read_u16 v98, v192 offset:6656
	ds_read_u16 v99, v192 offset:6672
	ds_read_u16 v100, v192 offset:6688
	ds_read_u16 v101, v192 offset:6704
	ds_read_u16 v102, v193 offset:1664
	ds_read_u16 v103, v193 offset:1680
	ds_read_u16 v104, v193 offset:1696
	ds_read_u16 v105, v193 offset:1712
	s_waitcnt lgkmcnt(8)
	v_lshl_or_b32 v232, v83, 16, v82
	v_lshl_or_b32 v233, v85, 16, v84
	s_mov_b64 exec, s[36:37]
	v_lshl_or_b32 v234, v91, 16, v90
	v_lshl_or_b32 v235, v93, 16, v92
	s_mov_b64 exec, -1
	ds_read_u16 v82, v192 offset:7168
	ds_read_u16 v83, v192 offset:7184
	ds_read_u16 v84, v192 offset:7200
	ds_read_u16 v85, v192 offset:7216
	ds_read_u16 v90, v193 offset:1792
	ds_read_u16 v91, v193 offset:1808
	ds_read_u16 v92, v193 offset:1824
	ds_read_u16 v93, v193 offset:1840
	s_waitcnt lgkmcnt(8)
	v_lshl_or_b32 v236, v99, 16, v98
	v_lshl_or_b32 v237, v101, 16, v100
	s_mov_b64 exec, s[36:37]
	v_lshl_or_b32 v238, v103, 16, v102
	v_lshl_or_b32 v239, v105, 16, v104
	s_mov_b64 exec, -1
	ds_read_u16 v98, v192 offset:7680
	ds_read_u16 v99, v192 offset:7696
	ds_read_u16 v100, v192 offset:7712
	ds_read_u16 v101, v192 offset:7728
	ds_read_u16 v102, v193 offset:1920
	ds_read_u16 v103, v193 offset:1936
	ds_read_u16 v104, v193 offset:1952
	ds_read_u16 v105, v193 offset:1968
	s_waitcnt lgkmcnt(8)
	v_lshl_or_b32 v240, v83, 16, v82
	v_lshl_or_b32 v241, v85, 16, v84
	s_mov_b64 exec, s[36:37]
	v_lshl_or_b32 v242, v91, 16, v90
	v_lshl_or_b32 v243, v93, 16, v92
	s_mov_b64 exec, -1
	s_waitcnt lgkmcnt(0)
	v_lshl_or_b32 v244, v99, 16, v98
	v_lshl_or_b32 v245, v101, 16, v100
	s_mov_b64 exec, s[36:37]
	v_lshl_or_b32 v246, v103, 16, v102
	v_lshl_or_b32 v247, v105, 16, v104
	s_mov_b64 exec, -1
	s_waitcnt lgkmcnt(0)
	s_mov_b64 exec, s[38:39]
	v_cvt_pk_bf16_f32 v66, v2, v195
	v_cvt_pk_bf16_f32 v74, v3, v195
	v_lshlrev_b32_e32 v67, 16, v66
	v_lshlrev_b32_e32 v75, 16, v74
	v_sub_f32_e32 v2, v2, v67
	v_sub_f32_e32 v3, v3, v75
	v_cvt_pk_bf16_f32 v68, v2, v195
	v_cvt_pk_bf16_f32 v76, v3, v195
	v_lshlrev_b32_e32 v69, 16, v68
	v_lshlrev_b32_e32 v77, 16, v76
	v_sub_f32_e32 v2, v2, v69
	v_sub_f32_e32 v3, v3, v77
	v_cvt_pk_bf16_f32 v147, v2, v195
	v_cvt_pk_bf16_f32 v151, v3, v195
	v_cvt_pk_bf16_f32 v146, v67, v69
	v_cvt_pk_bf16_f32 v150, v75, v77
	v_cvt_pk_bf16_f32 v66, v4, v195
	v_cvt_pk_bf16_f32 v74, v5, v195
	v_lshlrev_b32_e32 v67, 16, v66
	v_lshlrev_b32_e32 v75, 16, v74
	v_sub_f32_e32 v4, v4, v67
	v_sub_f32_e32 v5, v5, v75
	v_cvt_pk_bf16_f32 v68, v4, v195
	v_cvt_pk_bf16_f32 v76, v5, v195
	v_lshlrev_b32_e32 v69, 16, v68
	v_lshlrev_b32_e32 v77, 16, v76
	v_sub_f32_e32 v4, v4, v69
	v_sub_f32_e32 v5, v5, v77
	v_cvt_pk_bf16_f32 v155, v4, v195
	v_cvt_pk_bf16_f32 v159, v5, v195
	v_cvt_pk_bf16_f32 v154, v67, v69
	v_cvt_pk_bf16_f32 v158, v75, v77
	v_cvt_pk_bf16_f32 v66, v6, v195
	v_cvt_pk_bf16_f32 v74, v7, v195
	v_lshlrev_b32_e32 v67, 16, v66
	v_lshlrev_b32_e32 v75, 16, v74
	v_sub_f32_e32 v6, v6, v67
	v_sub_f32_e32 v7, v7, v75
	v_cvt_pk_bf16_f32 v68, v6, v195
	v_cvt_pk_bf16_f32 v76, v7, v195
	v_lshlrev_b32_e32 v69, 16, v68
	v_lshlrev_b32_e32 v77, 16, v76
	v_sub_f32_e32 v6, v6, v69
	v_sub_f32_e32 v7, v7, v77
	v_cvt_pk_bf16_f32 v163, v6, v195
	v_cvt_pk_bf16_f32 v167, v7, v195
	v_cvt_pk_bf16_f32 v162, v67, v69
	v_cvt_pk_bf16_f32 v166, v75, v77
	v_cvt_pk_bf16_f32 v66, v8, v195
	v_cvt_pk_bf16_f32 v74, v9, v195
	v_lshlrev_b32_e32 v67, 16, v66
	v_lshlrev_b32_e32 v75, 16, v74
	v_sub_f32_e32 v8, v8, v67
	v_sub_f32_e32 v9, v9, v75
	v_cvt_pk_bf16_f32 v68, v8, v195
	v_cvt_pk_bf16_f32 v76, v9, v195
	v_lshlrev_b32_e32 v69, 16, v68
	v_lshlrev_b32_e32 v77, 16, v76
	v_sub_f32_e32 v8, v8, v69
	v_sub_f32_e32 v9, v9, v77
	v_cvt_pk_bf16_f32 v171, v8, v195
	v_cvt_pk_bf16_f32 v175, v9, v195
	v_cvt_pk_bf16_f32 v170, v67, v69
	v_cvt_pk_bf16_f32 v174, v75, v77
	v_cvt_pk_bf16_f32 v66, v50, v195
	v_cvt_pk_bf16_f32 v74, v51, v195
	v_lshlrev_b32_e32 v67, 16, v66
	v_lshlrev_b32_e32 v75, 16, v74
	v_sub_f32_e32 v50, v50, v67
	v_sub_f32_e32 v51, v51, v75
	v_cvt_pk_bf16_f32 v68, v50, v195
	v_cvt_pk_bf16_f32 v76, v51, v195
	v_lshlrev_b32_e32 v69, 16, v68
	v_lshlrev_b32_e32 v77, 16, v76
	v_sub_f32_e32 v50, v50, v69
	v_sub_f32_e32 v51, v51, v77
	v_cvt_pk_bf16_f32 v179, v50, v195
	v_cvt_pk_bf16_f32 v183, v51, v195
	v_cvt_pk_bf16_f32 v178, v67, v69
	v_cvt_pk_bf16_f32 v182, v75, v77
	v_cvt_pk_bf16_f32 v66, v52, v195
	v_cvt_pk_bf16_f32 v74, v53, v195
	v_lshlrev_b32_e32 v67, 16, v66
	v_lshlrev_b32_e32 v75, 16, v74
	v_sub_f32_e32 v52, v52, v67
	v_sub_f32_e32 v53, v53, v75
	v_cvt_pk_bf16_f32 v68, v52, v195
	v_cvt_pk_bf16_f32 v76, v53, v195
	v_lshlrev_b32_e32 v69, 16, v68
	v_lshlrev_b32_e32 v77, 16, v76
	v_sub_f32_e32 v52, v52, v69
	v_sub_f32_e32 v53, v53, v77
	v_cvt_pk_bf16_f32 v187, v52, v195
	v_cvt_pk_bf16_f32 v191, v53, v195
	v_cvt_pk_bf16_f32 v186, v67, v69
	v_cvt_pk_bf16_f32 v190, v75, v77
	v_cvt_pk_bf16_f32 v66, v58, v195
	v_cvt_pk_bf16_f32 v74, v59, v195
	v_lshlrev_b32_e32 v67, 16, v66
	v_lshlrev_b32_e32 v75, 16, v74
	v_sub_f32_e32 v58, v58, v67
	v_sub_f32_e32 v59, v59, v75
	v_cvt_pk_bf16_f32 v68, v58, v195
	v_cvt_pk_bf16_f32 v76, v59, v195
	v_lshlrev_b32_e32 v69, 16, v68
	v_lshlrev_b32_e32 v77, 16, v76
	v_sub_f32_e32 v58, v58, v69
	v_sub_f32_e32 v59, v59, v77
	v_cvt_pk_bf16_f32 v235, v58, v195
	v_cvt_pk_bf16_f32 v239, v59, v195
	v_cvt_pk_bf16_f32 v234, v67, v69
	v_cvt_pk_bf16_f32 v238, v75, v77
	v_cvt_pk_bf16_f32 v66, v60, v195
	v_cvt_pk_bf16_f32 v74, v61, v195
	v_lshlrev_b32_e32 v67, 16, v66
	v_lshlrev_b32_e32 v75, 16, v74
	v_sub_f32_e32 v60, v60, v67
	v_sub_f32_e32 v61, v61, v75
	v_cvt_pk_bf16_f32 v68, v60, v195
	v_cvt_pk_bf16_f32 v76, v61, v195
	v_lshlrev_b32_e32 v69, 16, v68
	v_lshlrev_b32_e32 v77, 16, v76
	v_sub_f32_e32 v60, v60, v69
	v_sub_f32_e32 v61, v61, v77
	v_cvt_pk_bf16_f32 v243, v60, v195
	v_cvt_pk_bf16_f32 v247, v61, v195
	v_cvt_pk_bf16_f32 v242, v67, v69
	v_cvt_pk_bf16_f32 v246, v75, v77
	s_mov_b64 exec, -1
	s_movk_i32 s44, 0x210
	v_and_b32_e32 v192, 48, v0
	v_lshrrev_b32_e32 v193, 5, v1
	v_mad_u32_u24 v214, v197, s44, v199
	v_mad_u32_u24 v215, v193, s44, v199
	v_add_u32_e32 v214, v214, v192
	v_and_b32_e32 v192, 0x1f0, v194
	v_add_u32_e32 v215, v215, v192
	s_and_b32 s44, s2, 7
	s_lshl_b32 s44, s44, 22
	s_lshl_b32 s45, s3, 17
	s_add_i32 s44, s44, s45
	v_lshlrev_b32_e32 v220, 13, v193
	v_or3_b32 v220, s44, v220, v196
	v_add_u32_e32 v220, v220, v192
	v_or_b32_e32 v203, 0x24800, v198
	s_mov_b32 s12, 0
	s_mov_b32 s11, 0x20000
	s_brev_b32 s10, 8
	s_and_b32 s9, s9, 0xffff
	v_lshlrev_b32_e32 v192, 3, v142
	v_and_b32_e32 v192, 56, v192
	v_lshl_or_b32 v193, v192, 8, v204
	v_lshl_or_b32 v192, v192, 10, v198
	s_nop 4
	v_mfma_f32_16x16x32_bf16 v[2:5], v[26:29], v[42:45], v[18:21]
	s_nop 1
	ds_read_b128 v[58:61], v192
	ds_read_b128 v[110:113], v193
	ds_read_b128 v[50:53], v192 offset:1024
	ds_read_b128 v[118:121], v193 offset:256
	ds_read_b128 v[66:69], v192 offset:2048
	ds_read_b128 v[126:129], v193 offset:512
	ds_read_b128 v[74:77], v192 offset:3072
	ds_read_b128 v[134:137], v193 offset:768
	ds_read_b128 v[82:85], v192 offset:4096
	ds_read_b128 v[138:141], v193 offset:1024
	ds_read_b128 v[90:93], v192 offset:5120
	ds_read_b128 v[18:21], v193 offset:1280
	ds_read_b128 v[98:101], v192 offset:6144
	ds_read_b128 v[26:29], v193 offset:1536
	ds_read_b128 v[102:105], v192 offset:7168
	ds_read_b128 v[42:45], v193 offset:1792
	s_waitcnt vmcnt(15)
	v_cvt_pk_bf16_f32 v6, v10, v11
	v_cvt_pk_bf16_f32 v7, v12, v13
	ds_write_b64 v212, v[6:7]
	s_waitcnt vmcnt(14)
	v_cvt_pk_bf16_f32 v6, v14, v15
	v_cvt_pk_bf16_f32 v7, v16, v17
	ds_write_b64 v211, v[6:7] offset:512
	s_waitcnt vmcnt(13)
	v_cvt_pk_bf16_f32 v6, v22, v23
	v_cvt_pk_bf16_f32 v7, v24, v25
	ds_write_b64 v210, v[6:7] offset:1024
	s_waitcnt vmcnt(12)
	v_cvt_pk_bf16_f32 v6, v30, v31
	v_cvt_pk_bf16_f32 v7, v32, v33
	ds_write_b64 v209, v[6:7] offset:1536
	s_waitcnt vmcnt(11)
	v_cvt_pk_bf16_f32 v6, v38, v39
	v_cvt_pk_bf16_f32 v7, v40, v41
	ds_write_b64 v208, v[6:7] offset:2048
	s_waitcnt vmcnt(10)
	v_cvt_pk_bf16_f32 v6, v46, v47
	v_cvt_pk_bf16_f32 v7, v48, v49
	ds_write_b64 v207, v[6:7] offset:2560
	s_waitcnt vmcnt(9)
	v_cvt_pk_bf16_f32 v6, v54, v55
	v_cvt_pk_bf16_f32 v7, v56, v57
	ds_write_b64 v206, v[6:7] offset:3072
	s_waitcnt vmcnt(8)
	v_cvt_pk_bf16_f32 v6, v62, v63
	v_cvt_pk_bf16_f32 v7, v64, v65
	ds_write_b64 v205, v[6:7] offset:3584
	s_waitcnt vmcnt(7)
	v_cvt_pk_bf16_f32 v6, v70, v71
	v_cvt_pk_bf16_f32 v7, v72, v73
	ds_write_b64 v231, v[6:7] offset:4096
	s_waitcnt vmcnt(6)
	v_cvt_pk_bf16_f32 v6, v78, v79
	v_cvt_pk_bf16_f32 v7, v80, v81
	ds_write_b64 v230, v[6:7] offset:4608
	s_waitcnt vmcnt(5)
	v_cvt_pk_bf16_f32 v6, v86, v87
	v_cvt_pk_bf16_f32 v7, v88, v89
	ds_write_b64 v229, v[6:7] offset:5120
	s_waitcnt vmcnt(4)
	v_cvt_pk_bf16_f32 v6, v94, v95
	v_cvt_pk_bf16_f32 v7, v96, v97
	ds_write_b64 v228, v[6:7] offset:5632
	s_waitcnt vmcnt(3)
	v_cvt_pk_bf16_f32 v6, v106, v107
	v_cvt_pk_bf16_f32 v7, v108, v109
	ds_write_b64 v227, v[6:7] offset:6144
	s_waitcnt vmcnt(2)
	v_cvt_pk_bf16_f32 v6, v114, v115
	v_cvt_pk_bf16_f32 v7, v116, v117
	ds_write_b64 v226, v[6:7] offset:6656
	s_waitcnt vmcnt(1)
	v_cvt_pk_bf16_f32 v6, v122, v123
	v_cvt_pk_bf16_f32 v7, v124, v125
	ds_write_b64 v225, v[6:7] offset:7168
	s_waitcnt vmcnt(0)
	v_cvt_pk_bf16_f32 v6, v130, v131
	v_cvt_pk_bf16_f32 v7, v132, v133
	ds_write_b64 v224, v[6:7] offset:7680
	ds_read_b128 v[54:57], v223
	ds_read_b128 v[62:65], v222
	ds_read_b128 v[10:13], v221
	ds_read_b128 v[14:17], v219
	ds_read_b128 v[22:25], v218
	ds_read_b128 v[30:33], v217
	ds_read_b128 v[38:41], v216
	ds_read_b128 v[46:49], v213
	s_waitcnt lgkmcnt(7)
	v_mfma_f32_16x16x32_bf16 v[34:37], v[58:61], v[54:57], v[34:37]
	v_mfma_f32_16x16x32_bf16 v[2:5], v[110:113], v[54:57], v[2:5]
	s_waitcnt lgkmcnt(6)
	v_mfma_f32_16x16x32_bf16 v[34:37], v[50:53], v[62:65], v[34:37]
	v_mfma_f32_16x16x32_bf16 v[2:5], v[118:121], v[62:65], v[2:5]
	s_waitcnt lgkmcnt(5)
	v_mfma_f32_16x16x32_bf16 v[34:37], v[66:69], v[10:13], v[34:37]
	v_mfma_f32_16x16x32_bf16 v[2:5], v[126:129], v[10:13], v[2:5]
	s_waitcnt lgkmcnt(4)
	v_mfma_f32_16x16x32_bf16 v[34:37], v[74:77], v[14:17], v[34:37]
	v_mfma_f32_16x16x32_bf16 v[2:5], v[134:137], v[14:17], v[2:5]
	s_waitcnt lgkmcnt(3)
	v_mfma_f32_16x16x32_bf16 v[34:37], v[82:85], v[22:25], v[34:37]
	v_mfma_f32_16x16x32_bf16 v[2:5], v[138:141], v[22:25], v[2:5]
	s_waitcnt lgkmcnt(2)
	v_mfma_f32_16x16x32_bf16 v[34:37], v[90:93], v[30:33], v[34:37]
	v_mfma_f32_16x16x32_bf16 v[2:5], v[18:21], v[30:33], v[2:5]
	s_waitcnt lgkmcnt(1)
	v_mfma_f32_16x16x32_bf16 v[34:37], v[98:101], v[38:41], v[34:37]
	v_mfma_f32_16x16x32_bf16 v[2:5], v[26:29], v[38:41], v[2:5]
	s_waitcnt lgkmcnt(0)
	v_mfma_f32_16x16x32_bf16 v[56:59], v[102:105], v[46:49], v[34:37]
	v_mfma_f32_16x16x32_bf16 v[60:63], v[42:45], v[46:49], v[2:5]
	v_add_u32_e32 v76, 0x24800, v196
	s_waitcnt lgkmcnt(0)
	v_cmp_gt_u32_e64 s[0:1], 16, v1
	v_cmp_lt_u32_e32 vcc, 15, v1
	s_waitcnt lgkmcnt(0)
	s_nop 2
	v_max_f32_e32 v2, v59, v59
	v_max_f32_e32 v3, v58, v58
	s_waitcnt lgkmcnt(0)
	v_max_f32_e32 v2, v3, v2
	s_nop 0
	s_nop 0
	s_nop 0
	s_waitcnt lgkmcnt(0)
	s_nop 0
	s_nop 0
	s_and_saveexec_b64 s[4:5], vcc
	s_xor_b64 s[4:5], exec, s[4:5]
	s_or_saveexec_b64 s[4:5], s[4:5]
	v_max3_f32 v53, v56, v57, v2
	s_xor_b64 exec, exec, s[4:5]
	v_max_f32_e32 v2, v61, v61
	v_max_f32_e32 v3, v60, v60
	v_max_f32_e32 v2, v3, v2
	v_max_f32_e32 v3, v63, v63
	v_max_f32_e32 v4, v62, v62
	v_max_f32_e32 v3, v4, v3
	v_max3_f32 v53, v53, v2, v3
	s_or_b64 exec, exec, s[4:5]
	v_cmp_eq_u32_e64 s[4:5], 1, v201
	v_max_f32_e32 v53, v53, v53
	v_mov_b32_e32 v68, v53
	s_nop 1
	v_permlane16_swap_b32_e32 v53, v68
	v_max_f32_e32 v68, v53, v68
	v_mov_b32_e32 v55, v68
	s_nop 1
	v_permlane32_swap_b32_e32 v68, v55
	v_max_f32_e32 v68, v68, v55
	v_sub_f32_e32 v55, v56, v68
	v_mul_f32_e32 v55, 0x3fb8aa3b, v55
	v_exp_f32_e32 v70, v55
	v_sub_f32_e32 v55, v57, v68
	v_sub_f32_e32 v57, v59, v68
	v_mul_f32_e32 v57, 0x3fb8aa3b, v57
	v_mul_f32_e32 v55, 0x3fb8aa3b, v55
	v_exp_f32_e32 v59, v57
	v_sub_f32_e32 v57, v60, v68
	v_exp_f32_e32 v71, v55
	v_sub_f32_e32 v55, v58, v68
	v_mul_f32_e32 v57, 0x3fb8aa3b, v57
	v_sub_f32_e32 v58, v61, v68
	v_exp_f32_e32 v57, v57
	v_mul_f32_e32 v58, 0x3fb8aa3b, v58
	v_exp_f32_e32 v58, v58
	v_mul_f32_e32 v55, 0x3fb8aa3b, v55
	v_exp_f32_e32 v72, v55
	v_cndmask_b32_e64 v60, 0, v57, s[0:1]
	v_sub_f32_e32 v57, v62, v68
	v_add_f32_e32 v56, 0, v70
	v_cndmask_b32_e64 v61, 0, v58, s[0:1]
	v_mul_f32_e32 v57, 0x3fb8aa3b, v57
	v_sub_f32_e32 v58, v63, v68
	v_add_f32_e32 v56, v56, v71
	v_exp_f32_e32 v57, v57
	v_mul_f32_e32 v58, 0x3fb8aa3b, v58
	v_add_f32_e32 v56, v56, v72
	v_exp_f32_e32 v58, v58
	v_add_f32_e32 v56, v56, v59
	v_add_f32_e32 v56, v56, v60
	v_add_f32_e32 v56, v56, v61
	v_cndmask_b32_e64 v62, 0, v57, s[0:1]
	v_add_f32_e32 v56, v56, v62
	v_cndmask_b32_e64 v63, 0, v58, s[0:1]
	v_add_f32_e32 v57, v56, v63
	v_mov_b32_e32 v58, v57
	s_nop 1
	v_permlane16_swap_b32_e32 v57, v58
	v_add_f32_e32 v58, v57, v58
	v_mov_b32_e32 v68, v58
	s_nop 1
	v_permlane32_swap_b32_e32 v58, v68
	v_add_f32_e32 v68, v58, v68
	v_div_scale_f32 v69, s[6:7], v68, v68, 1.0
	v_rcp_f32_e32 v73, v69
	s_nop 0
	v_fma_f32 v75, -v69, v73, 1.0
	v_fmac_f32_e32 v73, v75, v73
	v_div_scale_f32 v75, vcc, 1.0, v68, 1.0
	v_mul_f32_e32 v92, v75, v73
	v_fma_f32 v93, -v69, v92, v75
	v_fmac_f32_e32 v92, v93, v73
	v_fma_f32 v69, -v69, v92, v75
	v_div_fmas_f32 v69, v69, v73, v92
	v_div_fixup_f32 v68, v69, v68, 1.0
	v_mul_f32_e32 v69, v68, v70
	v_mov_b32_e32 v75, 0xbb23d70a
	v_mov_b32_e32 v73, 0x3b23d70a
	v_fmaak_f32 v92, v68, v70, 0xbb23d70a
	v_fmaak_f32 v70, v68, v70, 0x3b23d70a
	v_cmp_lt_f32_e32 vcc, v69, v75
	v_fmaak_f32 v93, v68, v60, 0xbb23d70a
	s_nop 0
	v_cndmask_b32_e32 v70, 0, v70, vcc
	v_cmp_gt_f32_e32 vcc, v69, v73
	s_nop 1
	v_cndmask_b32_e32 v69, v70, v92, vcc
	v_mul_f32_e32 v92, v68, v60
	v_fmaak_f32 v60, v68, v60, 0x3b23d70a
	v_cmp_lt_f32_e32 vcc, v92, v75
	v_max_f32_e32 v70, 0xf149f2ca, v69
	s_nop 0
	v_cndmask_b32_e32 v60, 0, v60, vcc
	v_cmp_gt_f32_e32 vcc, v92, v73
	s_nop 1
	v_cndmask_b32_e32 v92, v60, v93, vcc
	v_max_f32_e32 v60, v70, v92
	v_cndmask_b32_e64 v60, v70, v60, s[0:1]
	v_mul_f32_e32 v70, v68, v71
	v_fmaak_f32 v93, v68, v71, 0xbb23d70a
	v_fmaak_f32 v71, v68, v71, 0x3b23d70a
	v_cmp_lt_f32_e32 vcc, v70, v75
	s_nop 1
	v_cndmask_b32_e32 v71, 0, v71, vcc
	v_cmp_gt_f32_e32 vcc, v70, v73
	s_nop 1
	v_cndmask_b32_e32 v70, v71, v93, vcc
	v_mul_f32_e32 v71, v68, v61
	v_fmaak_f32 v93, v68, v61, 0xbb23d70a
	v_fmaak_f32 v61, v68, v61, 0x3b23d70a
	v_cmp_lt_f32_e32 vcc, v71, v75
	v_max_f32_e32 v60, v60, v70
	s_nop 0
	v_cndmask_b32_e32 v61, 0, v61, vcc
	v_cmp_gt_f32_e32 vcc, v71, v73
	s_nop 1
	v_cndmask_b32_e32 v71, v61, v93, vcc
	v_max_f32_e32 v61, v60, v71
	v_cndmask_b32_e64 v60, v60, v61, s[0:1]
	v_mul_f32_e32 v61, v68, v72
	v_fmaak_f32 v93, v68, v72, 0xbb23d70a
	v_fmaak_f32 v72, v68, v72, 0x3b23d70a
	v_cmp_lt_f32_e32 vcc, v61, v75
	s_nop 1
	v_cndmask_b32_e32 v72, 0, v72, vcc
	v_cmp_gt_f32_e32 vcc, v61, v73
	v_mul_f32_e32 v61, v68, v62
	s_nop 0
	v_cndmask_b32_e32 v72, v72, v93, vcc
	v_fmaak_f32 v93, v68, v62, 0xbb23d70a
	v_fmaak_f32 v62, v68, v62, 0x3b23d70a
	v_cmp_lt_f32_e32 vcc, v61, v75
	v_max_f32_e32 v60, v60, v72
	s_nop 0
	v_cndmask_b32_e32 v62, 0, v62, vcc
	v_cmp_gt_f32_e32 vcc, v61, v73
	s_nop 1
	v_cndmask_b32_e32 v62, v62, v93, vcc
	v_max_f32_e32 v61, v60, v62
	v_cndmask_b32_e64 v60, v60, v61, s[0:1]
	v_mul_f32_e32 v61, v68, v59
	v_fmaak_f32 v93, v68, v59, 0xbb23d70a
	v_fmaak_f32 v59, v68, v59, 0x3b23d70a
	v_cmp_lt_f32_e32 vcc, v61, v75
	s_nop 1
	v_cndmask_b32_e32 v59, 0, v59, vcc
	v_cmp_gt_f32_e32 vcc, v61, v73
	s_nop 1
	v_cndmask_b32_e32 v93, v59, v93, vcc
	v_max_f32_e32 v59, v60, v93
	v_mul_f32_e32 v60, v68, v63
	v_cmp_gt_f32_e32 vcc, v60, v73
	v_fmac_f32_e32 v73, v68, v63
	v_cmp_lt_f32_e64 s[6:7], v60, v75
	v_fmac_f32_e32 v75, v68, v63
	s_nop 0
	v_cndmask_b32_e64 v60, 0, v73, s[6:7]
	v_cndmask_b32_e32 v63, v60, v75, vcc
	v_max_f32_e32 v60, v59, v63
	v_cndmask_b32_e64 v60, v59, v60, s[0:1]
	v_mov_b32_e32 v61, v60
	s_nop 1
	v_permlane16_swap_b32_e32 v60, v61
	v_max_f32_e32 v61, v60, v61
	v_mov_b32_e32 v74, v61
	s_nop 1
	v_permlane32_swap_b32_e32 v61, v74
	v_max_f32_e32 v74, v61, v74
	v_sub_f32_e32 v61, v69, v74
	v_mul_f32_e32 v61, 0x3fb8aa3b, v61
	v_exp_f32_e32 v69, v61
	v_sub_f32_e32 v61, v92, v74
	v_mul_f32_e32 v61, 0x3fb8aa3b, v61
	v_exp_f32_e32 v75, v61
	v_sub_f32_e32 v70, v70, v74
	v_sub_f32_e32 v71, v71, v74
	v_mul_f32_e32 v70, 0x3fb8aa3b, v70
	v_mul_f32_e32 v71, 0x3fb8aa3b, v71
	v_exp_f32_e32 v70, v70
	v_exp_f32_e32 v71, v71
	v_sub_f32_e32 v72, v72, v74
	v_sub_f32_e32 v62, v62, v74
	v_mul_f32_e32 v72, 0x3fb8aa3b, v72
	v_mul_f32_e32 v62, 0x3fb8aa3b, v62
	v_add_f32_e32 v73, 0, v69
	v_cndmask_b32_e64 v75, 0, v75, s[0:1]
	v_exp_f32_e32 v72, v72
	v_exp_f32_e32 v62, v62
	v_sub_f32_e32 v84, v93, v74
	v_sub_f32_e32 v63, v63, v74
	v_add_f32_e32 v73, v73, v75
	v_mul_f32_e32 v84, 0x3fb8aa3b, v84
	v_mul_f32_e32 v63, 0x3fb8aa3b, v63
	v_add_f32_e32 v73, v73, v70
	v_cndmask_b32_e64 v71, 0, v71, s[0:1]
	v_exp_f32_e32 v84, v84
	v_exp_f32_e32 v63, v63
	v_add_f32_e32 v73, v73, v71
	v_add_f32_e32 v73, v73, v72
	v_cndmask_b32_e64 v74, 0, v62, s[0:1]
	v_add_f32_e32 v62, v73, v74
	v_add_f32_e32 v62, v62, v84
	v_cndmask_b32_e64 v73, 0, v63, s[0:1]
	v_add_f32_e32 v85, v62, v73
	v_mov_b32_e32 v66, v85
	s_nop 1
	v_permlane16_swap_b32_e32 v85, v66
	v_add_f32_e32 v66, v85, v66
	v_mov_b32_e32 v67, v66
	s_nop 1
	v_permlane32_swap_b32_e32 v66, v67
	v_add_f32_e32 v66, v66, v67
	v_div_scale_f32 v67, s[6:7], v66, v66, 1.0
	v_rcp_f32_e32 v78, v67
	s_nop 0
	v_fma_f32 v68, -v67, v78, 1.0
	v_fmac_f32_e32 v78, v68, v78
	v_div_scale_f32 v68, vcc, 1.0, v66, 1.0
	v_mul_f32_e32 v77, v68, v78
	v_fma_f32 v79, -v67, v77, v68
	v_fmac_f32_e32 v77, v79, v78
	v_fma_f32 v67, -v67, v77, v68
	v_div_fmas_f32 v67, v67, v78, v77
	v_div_fixup_f32 v66, v67, v66, 1.0
	v_mov_b32_e32 v67, 0xbd4ccccd
	v_fmaak_f32 v68, v66, v69, 0xbd4ccccd
	v_fmaak_f32 v69, v66, v70, 0xbd4ccccd
	v_fmaak_f32 v70, v66, v72, 0xbd4ccccd
	v_fmaak_f32 v75, v66, v75, 0xbd4ccccd
	v_fmaak_f32 v71, v66, v71, 0xbd4ccccd
	v_fmaak_f32 v74, v66, v74, 0xbd4ccccd
	v_mul_f32_e32 v70, 0x4038aa3b, v70
	v_fmaak_f32 v72, v66, v84, 0xbd4ccccd
	v_mul_f32_e32 v75, 0x4038aa3b, v75
	v_mul_f32_e32 v71, 0x4038aa3b, v71
	v_mul_f32_e32 v74, 0x4038aa3b, v74
	v_fmac_f32_e32 v67, v66, v73
	v_mul_f32_e32 v68, 0x4038aa3b, v68
	v_mul_f32_e32 v69, 0x4038aa3b, v69
	v_mul_f32_e32 v72, 0x4038aa3b, v72
	v_cndmask_b32_e64 v75, 0, v75, s[0:1]
	v_cndmask_b32_e64 v71, 0, v71, s[0:1]
	v_cndmask_b32_e64 v74, 0, v74, s[0:1]
	v_mul_f32_e32 v66, 0x4038aa3b, v67
	v_cvt_pk_bf16_f32 v67, v70, v72
	v_add_u32_e32 v70, v76, v198
	v_cndmask_b32_e64 v73, 0, v66, s[0:1]
	v_cndmask_b32_e64 v74, v74, 1.0, s[4:5]
	v_cndmask_b32_e64 v75, v75, 1.0, s[4:5]
	v_cndmask_b32_e64 v71, v71, 1.0, s[4:5]
	v_cvt_pk_bf16_f32 v66, v68, v69
	v_cvt_pk_bf16_f32 v68, v75, v71
	v_cvt_pk_bf16_f32 v69, v74, v73
	ds_write_b128 v70, v[66:69]
	s_waitcnt lgkmcnt(0)
	s_barrier
	ds_read_b128 v[2:5], v203
	v_add_u32_e32 v6, 0x1c00, v203
	v_mov_b32_e32 v132, v220
	v_add_u32_e32 v133, 0x4000, v220
	v_add_u32_e32 v134, 0x8000, v220
	v_add_u32_e32 v135, 0xc000, v220
	v_add_u32_e32 v136, 0x10000, v220
	v_add_u32_e32 v137, 0x14000, v220
	v_add_u32_e32 v138, 0x18000, v220
	v_add_u32_e32 v139, 0x1c000, v220
.LBB0_3:
	s_mov_b32 s13, s12
	s_add_i32 s12, s12, 0x2000000
	v_add_u32_e32 v203, 0x400, v203
	s_cmp_eq_u32 s12, 0x10000000
	v_min_u32_e32 v203, v203, v6
	s_waitcnt lgkmcnt(0)
	v_mfma_f32_16x16x32_bf16 v[66:69], v[144:147], v[2:5], 0
	v_mfma_f32_16x16x32_bf16 v[74:77], v[148:151], v[2:5], 0
	s_nop 2
	s_nop 3
	v_exp_f32_e32 v66, v66
	v_exp_f32_e32 v67, v67
	v_mfma_f32_16x16x32_bf16 v[78:81], v[152:155], v[2:5], 0
	v_exp_f32_e32 v68, v68
	v_exp_f32_e32 v69, v69
	v_exp_f32_e32 v74, v74
	v_mfma_f32_16x16x32_bf16 v[82:85], v[156:159], v[2:5], 0
	v_exp_f32_e32 v75, v75
	v_exp_f32_e32 v76, v76
	v_exp_f32_e32 v77, v77
	v_mfma_f32_16x16x32_bf16 v[86:89], v[160:163], v[2:5], 0
	v_exp_f32_e32 v78, v78
	v_exp_f32_e32 v79, v79
	v_exp_f32_e32 v80, v80
	v_mfma_f32_16x16x32_bf16 v[90:93], v[164:167], v[2:5], 0
	v_exp_f32_e32 v81, v81
	v_exp_f32_e32 v82, v82
	v_exp_f32_e32 v83, v83
	v_mfma_f32_16x16x32_bf16 v[94:97], v[168:171], v[2:5], 0
	v_exp_f32_e32 v84, v84
	v_exp_f32_e32 v85, v85
	v_exp_f32_e32 v86, v86
	v_mfma_f32_16x16x32_bf16 v[98:101], v[172:175], v[2:5], 0
	v_exp_f32_e32 v87, v87
	v_exp_f32_e32 v88, v88
	v_exp_f32_e32 v89, v89
	v_mfma_f32_16x16x32_bf16 v[102:105], v[176:179], v[2:5], 0
	v_exp_f32_e32 v90, v90
	v_exp_f32_e32 v91, v91
	v_exp_f32_e32 v92, v92
	v_mfma_f32_16x16x32_bf16 v[108:111], v[180:183], v[2:5], 0
	v_exp_f32_e32 v93, v93
	v_exp_f32_e32 v94, v94
	v_exp_f32_e32 v95, v95
	v_mfma_f32_16x16x32_bf16 v[112:115], v[184:187], v[2:5], 0
	v_exp_f32_e32 v96, v96
	v_exp_f32_e32 v97, v97
	v_exp_f32_e32 v98, v98
	v_mfma_f32_16x16x32_bf16 v[116:119], v[188:191], v[2:5], 0
	v_exp_f32_e32 v99, v99
	v_exp_f32_e32 v100, v100
	v_exp_f32_e32 v101, v101
	v_mfma_f32_16x16x32_bf16 v[120:123], v[232:235], v[2:5], 0
	v_exp_f32_e32 v102, v102
	v_exp_f32_e32 v103, v103
	v_exp_f32_e32 v104, v104
	v_mfma_f32_16x16x32_bf16 v[124:127], v[236:239], v[2:5], 0
	v_exp_f32_e32 v105, v105
	v_exp_f32_e32 v108, v108
	v_exp_f32_e32 v109, v109
	v_mfma_f32_16x16x32_bf16 v[128:131], v[240:243], v[2:5], 0
	v_exp_f32_e32 v110, v110
	v_exp_f32_e32 v111, v111
	v_exp_f32_e32 v112, v112
	v_mfma_f32_16x16x32_bf16 v[70:73], v[244:247], v[2:5], 0
	ds_read_b128 v[2:5], v203
	v_exp_f32_e32 v113, v113
	v_exp_f32_e32 v114, v114
	v_exp_f32_e32 v115, v115
	v_exp_f32_e32 v116, v116
	v_exp_f32_e32 v117, v117
	v_exp_f32_e32 v118, v118
	v_exp_f32_e32 v119, v119
	v_exp_f32_e32 v120, v120
	v_exp_f32_e32 v121, v121
	v_exp_f32_e32 v122, v122
	v_exp_f32_e32 v123, v123
	v_exp_f32_e32 v124, v124
	v_exp_f32_e32 v125, v125
	v_exp_f32_e32 v126, v126
	v_exp_f32_e32 v127, v127
	v_exp_f32_e32 v128, v128
	v_exp_f32_e32 v129, v129
	v_exp_f32_e32 v130, v130
	v_exp_f32_e32 v131, v131
	v_exp_f32_e32 v70, v70
	v_exp_f32_e32 v71, v71
	v_exp_f32_e32 v72, v72
	v_exp_f32_e32 v73, v73
	v_pk_add_f32 v[66:67], v[66:67], 1.0 op_sel_hi:[1,0]
	v_pk_add_f32 v[68:69], v[68:69], 1.0 op_sel_hi:[1,0]
	v_pk_add_f32 v[74:75], v[74:75], 1.0 op_sel_hi:[1,0]
	v_pk_add_f32 v[76:77], v[76:77], 1.0 op_sel_hi:[1,0]
	v_pk_add_f32 v[78:79], v[78:79], 1.0 op_sel_hi:[1,0]
	v_pk_add_f32 v[80:81], v[80:81], 1.0 op_sel_hi:[1,0]
	v_pk_add_f32 v[82:83], v[82:83], 1.0 op_sel_hi:[1,0]
	v_pk_add_f32 v[84:85], v[84:85], 1.0 op_sel_hi:[1,0]
	v_pk_add_f32 v[86:87], v[86:87], 1.0 op_sel_hi:[1,0]
	v_pk_add_f32 v[88:89], v[88:89], 1.0 op_sel_hi:[1,0]
	v_pk_add_f32 v[90:91], v[90:91], 1.0 op_sel_hi:[1,0]
	v_pk_add_f32 v[92:93], v[92:93], 1.0 op_sel_hi:[1,0]
	v_pk_add_f32 v[94:95], v[94:95], 1.0 op_sel_hi:[1,0]
	v_pk_add_f32 v[96:97], v[96:97], 1.0 op_sel_hi:[1,0]
	v_pk_add_f32 v[98:99], v[98:99], 1.0 op_sel_hi:[1,0]
	v_pk_add_f32 v[100:101], v[100:101], 1.0 op_sel_hi:[1,0]
	v_pk_add_f32 v[102:103], v[102:103], 1.0 op_sel_hi:[1,0]
	v_pk_add_f32 v[104:105], v[104:105], 1.0 op_sel_hi:[1,0]
	v_rcp_f32_e32 v66, v66
	v_rcp_f32_e32 v67, v67
	v_rcp_f32_e32 v68, v68
	v_rcp_f32_e32 v69, v69
	v_pk_add_f32 v[108:109], v[108:109], 1.0 op_sel_hi:[1,0]
	v_pk_add_f32 v[110:111], v[110:111], 1.0 op_sel_hi:[1,0]
	v_pk_add_f32 v[112:113], v[112:113], 1.0 op_sel_hi:[1,0]
	v_pk_add_f32 v[114:115], v[114:115], 1.0 op_sel_hi:[1,0]
	v_pk_add_f32 v[116:117], v[116:117], 1.0 op_sel_hi:[1,0]
	v_pk_add_f32 v[118:119], v[118:119], 1.0 op_sel_hi:[1,0]
	v_pk_add_f32 v[120:121], v[120:121], 1.0 op_sel_hi:[1,0]
	v_pk_add_f32 v[122:123], v[122:123], 1.0 op_sel_hi:[1,0]
	v_pk_add_f32 v[124:125], v[124:125], 1.0 op_sel_hi:[1,0]
	v_pk_add_f32 v[126:127], v[126:127], 1.0 op_sel_hi:[1,0]
	v_pk_add_f32 v[128:129], v[128:129], 1.0 op_sel_hi:[1,0]
	v_pk_add_f32 v[130:131], v[130:131], 1.0 op_sel_hi:[1,0]
	v_add_f32_e32 v140, 1.0, v70
	v_add_f32_e32 v141, 1.0, v71
	v_add_f32_e32 v142, 1.0, v72
	v_add_f32_e32 v143, 1.0, v73
	v_rcp_f32_e32 v70, v74
	v_rcp_f32_e32 v71, v75
	v_rcp_f32_e32 v72, v76
	v_rcp_f32_e32 v73, v77
	v_rcp_f32_e32 v74, v78
	v_rcp_f32_e32 v75, v79
	v_rcp_f32_e32 v76, v80
	v_rcp_f32_e32 v77, v81
	v_rcp_f32_e32 v78, v82
	v_rcp_f32_e32 v79, v83
	v_rcp_f32_e32 v80, v84
	v_rcp_f32_e32 v81, v85
	v_rcp_f32_e32 v82, v86
	v_rcp_f32_e32 v83, v87
	v_rcp_f32_e32 v84, v88
	v_rcp_f32_e32 v85, v89
	v_rcp_f32_e32 v86, v90
	v_rcp_f32_e32 v87, v91
	v_rcp_f32_e32 v88, v92
	v_rcp_f32_e32 v89, v93
	v_rcp_f32_e32 v90, v94
	v_rcp_f32_e32 v91, v95
	v_rcp_f32_e32 v92, v96
	v_rcp_f32_e32 v93, v97
	v_rcp_f32_e32 v94, v98
	v_rcp_f32_e32 v95, v99
	v_rcp_f32_e32 v96, v100
	v_rcp_f32_e32 v97, v101
	v_rcp_f32_e32 v98, v102
	v_rcp_f32_e32 v99, v103
	v_rcp_f32_e32 v100, v104
	v_rcp_f32_e32 v101, v105
	v_rcp_f32_e32 v102, v108
	v_rcp_f32_e32 v103, v109
	v_rcp_f32_e32 v104, v110
	v_rcp_f32_e32 v105, v111
	v_rcp_f32_e32 v108, v112
	v_rcp_f32_e32 v109, v113
	v_rcp_f32_e32 v110, v114
	v_rcp_f32_e32 v111, v115
	v_rcp_f32_e32 v112, v116
	v_rcp_f32_e32 v113, v117
	v_rcp_f32_e32 v114, v118
	v_rcp_f32_e32 v115, v119
	v_rcp_f32_e32 v116, v120
	v_rcp_f32_e32 v117, v121
	v_rcp_f32_e32 v118, v122
	v_rcp_f32_e32 v119, v123
	v_rcp_f32_e32 v120, v124
	v_rcp_f32_e32 v121, v125
	v_rcp_f32_e32 v122, v126
	v_rcp_f32_e32 v123, v127
	v_rcp_f32_e32 v124, v128
	v_rcp_f32_e32 v125, v129
	v_rcp_f32_e32 v126, v130
	v_rcp_f32_e32 v127, v131
	v_rcp_f32_e32 v128, v140
	v_rcp_f32_e32 v129, v141
	v_rcp_f32_e32 v130, v142
	v_rcp_f32_e32 v131, v143
	v_pk_fma_f32 v[66:67], v[66:67], -2.0, 1.0 op_sel_hi:[1,0,0]
	v_pk_fma_f32 v[68:69], v[68:69], -2.0, 1.0 op_sel_hi:[1,0,0]
	v_pk_fma_f32 v[70:71], v[70:71], -2.0, 1.0 op_sel_hi:[1,0,0]
	v_pk_fma_f32 v[72:73], v[72:73], -2.0, 1.0 op_sel_hi:[1,0,0]
	v_pk_fma_f32 v[74:75], v[74:75], -2.0, 1.0 op_sel_hi:[1,0,0]
	v_pk_fma_f32 v[76:77], v[76:77], -2.0, 1.0 op_sel_hi:[1,0,0]
	v_pk_fma_f32 v[78:79], v[78:79], -2.0, 1.0 op_sel_hi:[1,0,0]
	v_pk_fma_f32 v[80:81], v[80:81], -2.0, 1.0 op_sel_hi:[1,0,0]
	v_pk_fma_f32 v[82:83], v[82:83], -2.0, 1.0 op_sel_hi:[1,0,0]
	v_pk_fma_f32 v[84:85], v[84:85], -2.0, 1.0 op_sel_hi:[1,0,0]
	v_pk_fma_f32 v[86:87], v[86:87], -2.0, 1.0 op_sel_hi:[1,0,0]
	v_pk_fma_f32 v[88:89], v[88:89], -2.0, 1.0 op_sel_hi:[1,0,0]
	v_pk_fma_f32 v[90:91], v[90:91], -2.0, 1.0 op_sel_hi:[1,0,0]
	v_pk_fma_f32 v[92:93], v[92:93], -2.0, 1.0 op_sel_hi:[1,0,0]
	v_pk_fma_f32 v[94:95], v[94:95], -2.0, 1.0 op_sel_hi:[1,0,0]
	v_pk_fma_f32 v[96:97], v[96:97], -2.0, 1.0 op_sel_hi:[1,0,0]
	v_pk_fma_f32 v[98:99], v[98:99], -2.0, 1.0 op_sel_hi:[1,0,0]
	v_pk_fma_f32 v[100:101], v[100:101], -2.0, 1.0 op_sel_hi:[1,0,0]
	ds_write_b128 v214, v[66:69]
	ds_write_b128 v214, v[70:73] offset:64
	ds_write_b128 v214, v[74:77] offset:128
	ds_write_b128 v214, v[78:81] offset:192
	ds_write_b128 v214, v[82:85] offset:256
	ds_write_b128 v214, v[86:89] offset:320
	ds_write_b128 v214, v[90:93] offset:384
	ds_write_b128 v214, v[94:97] offset:448
	v_pk_fma_f32 v[102:103], v[102:103], -2.0, 1.0 op_sel_hi:[1,0,0]
	v_pk_fma_f32 v[104:105], v[104:105], -2.0, 1.0 op_sel_hi:[1,0,0]
	v_pk_fma_f32 v[108:109], v[108:109], -2.0, 1.0 op_sel_hi:[1,0,0]
	v_pk_fma_f32 v[110:111], v[110:111], -2.0, 1.0 op_sel_hi:[1,0,0]
	v_pk_fma_f32 v[112:113], v[112:113], -2.0, 1.0 op_sel_hi:[1,0,0]
	v_pk_fma_f32 v[114:115], v[114:115], -2.0, 1.0 op_sel_hi:[1,0,0]
	v_pk_fma_f32 v[116:117], v[116:117], -2.0, 1.0 op_sel_hi:[1,0,0]
	v_pk_fma_f32 v[118:119], v[118:119], -2.0, 1.0 op_sel_hi:[1,0,0]
	v_pk_fma_f32 v[120:121], v[120:121], -2.0, 1.0 op_sel_hi:[1,0,0]
	v_pk_fma_f32 v[122:123], v[122:123], -2.0, 1.0 op_sel_hi:[1,0,0]
	v_pk_fma_f32 v[124:125], v[124:125], -2.0, 1.0 op_sel_hi:[1,0,0]
	v_pk_fma_f32 v[126:127], v[126:127], -2.0, 1.0 op_sel_hi:[1,0,0]
	v_pk_fma_f32 v[128:129], v[128:129], -2.0, 1.0 op_sel_hi:[1,0,0]
	v_pk_fma_f32 v[130:131], v[130:131], -2.0, 1.0 op_sel_hi:[1,0,0]
	ds_read_b128 v[66:69], v215
	ds_read_b128 v[70:73], v215 offset:1056
	ds_read_b128 v[74:77], v215 offset:2112
	ds_read_b128 v[78:81], v215 offset:3168
	ds_read_b128 v[82:85], v215 offset:4224
	ds_read_b128 v[86:89], v215 offset:5280
	ds_read_b128 v[90:93], v215 offset:6336
	ds_read_b128 v[94:97], v215 offset:7392
	ds_write_b128 v214, v[98:101]
	ds_write_b128 v214, v[102:105] offset:64
	ds_write_b128 v214, v[108:111] offset:128
	ds_write_b128 v214, v[112:115] offset:192
	ds_write_b128 v214, v[116:119] offset:256
	ds_write_b128 v214, v[120:123] offset:320
	ds_write_b128 v214, v[124:127] offset:384
	ds_write_b128 v214, v[128:131] offset:448
	ds_read_b128 v[98:101], v215
	ds_read_b128 v[102:105], v215 offset:1056
	ds_read_b128 v[108:111], v215 offset:2112
	ds_read_b128 v[112:115], v215 offset:3168
	ds_read_b128 v[116:119], v215 offset:4224
	ds_read_b128 v[120:123], v215 offset:5280
	ds_read_b128 v[124:127], v215 offset:6336
	ds_read_b128 v[128:131], v215 offset:7392
	s_waitcnt lgkmcnt(14)
	buffer_store_dwordx4 v[66:69], v132, s[8:11], s13 offen sc0 nt sc1
	buffer_store_dwordx4 v[70:73], v133, s[8:11], s13 offen sc0 nt sc1
	buffer_store_dwordx4 v[74:77], v134, s[8:11], s13 offen sc0 nt sc1
	buffer_store_dwordx4 v[78:81], v135, s[8:11], s13 offen sc0 nt sc1
	buffer_store_dwordx4 v[82:85], v136, s[8:11], s13 offen sc0 nt sc1
	buffer_store_dwordx4 v[86:89], v137, s[8:11], s13 offen sc0 nt sc1
	buffer_store_dwordx4 v[90:93], v138, s[8:11], s13 offen sc0 nt sc1
	buffer_store_dwordx4 v[94:97], v139, s[8:11], s13 offen sc0 nt sc1
	s_waitcnt lgkmcnt(7)
	buffer_store_dwordx4 v[98:101], v132, s[8:11], s13 offen offset:512 sc0 nt sc1
	s_waitcnt lgkmcnt(6)
	buffer_store_dwordx4 v[102:105], v133, s[8:11], s13 offen offset:512 sc0 nt sc1
	s_waitcnt lgkmcnt(5)
	buffer_store_dwordx4 v[108:111], v134, s[8:11], s13 offen offset:512 sc0 nt sc1
	s_waitcnt lgkmcnt(4)
	buffer_store_dwordx4 v[112:115], v135, s[8:11], s13 offen offset:512 sc0 nt sc1
	s_waitcnt lgkmcnt(3)
	buffer_store_dwordx4 v[116:119], v136, s[8:11], s13 offen offset:512 sc0 nt sc1
	s_waitcnt lgkmcnt(2)
	buffer_store_dwordx4 v[120:123], v137, s[8:11], s13 offen offset:512 sc0 nt sc1
	s_waitcnt lgkmcnt(1)
	buffer_store_dwordx4 v[124:127], v138, s[8:11], s13 offen offset:512 sc0 nt sc1
	s_waitcnt lgkmcnt(0)
	buffer_store_dwordx4 v[128:131], v139, s[8:11], s13 offen offset:512 sc0 nt sc1
	s_cbranch_scc0 .LBB0_3
	s_endpgm
